# GEMM K-loops: loop-control SALU block (pointer increments, exit test) moved above the loop-back barrier (loop-edge edit, guide 7.11)
# baseline (speedup 1.0000x reference)
; #define PG8_STAGE(bufoff, gbase, voff) do { _Pragma("unroll") for (int _i = 0; _i < 2; ++_i) { unsigned keep_; \
;         asm volatile("s_mov_b32 %0, m0\n\ts_mov_b32 m0, %3\n\ts_nop 0\n\tglobal_load_lds_dwordx4 %1, %2\n\ts_mov_b32 m0, %0" : "=&s"(keep_) : "v"((voff)[_i]), "s"((const char*)(gbase)), "s"(ldsb + (unsigned)((bufoff) + _i * 8192)) : "memory"); } } while (0)
; #define PG8_LDA(dst, b, h) do { _Pragma("unroll") for (int m = 0; m < 4; ++m) _Pragma("unroll") for (int k = 0; k < 2; ++k) dst[m][k] = *(const PG8_LAS bf16x8*)(lds + PG8_SA(b, h) + aoff + m * 2048 + k * 1024); } while (0)
; #define PG8_LDB(dst, b, h) do { _Pragma("unroll") for (int n = 0; n < 2; ++n) _Pragma("unroll") for (int k = 0; k < 2; ++k) dst[n][k] = *(const PG8_LAS bf16x8*)(lds + PG8_SB(b, h) + boff + n * 2048 + k * 1024); } while (0)
; #define PG8_WAIT_V(n) asm volatile("s_waitcnt vmcnt(" #n ")" ::: "memory")
; #define PG8_WAIT_L(n) asm volatile("s_waitcnt lgkmcnt(" #n ")" ::: "memory")
; #define PG8_BAR __builtin_amdgcn_s_barrier()
; #define PG8_SCHED __builtin_amdgcn_sched_barrier(0)
; template <class Epi, class Sched, bool ALIGN_EPI, bool FP8 = false>
; __device__ __forceinline__ void gemm_phase(PG8_LAS unsigned char* lds, const Gemm g, const Sched& S, const Epi& E, const int wid, const int lane) {
;     ...
;         for (int t = 0; t < nt; t += 2) {
;             const bool last = (t == nt - 2);
;             const char* a1 = cA + (size_t)(t + 1) * kstep;
;             const char* a2 = last ? nA : cA + (size_t)(t + 2) * kstep; const char* b2 = last ? nB : cB + (size_t)(t + 2) * kstep;
;             const char* a3 = a2 + kstep; const char* b3 = b2 + kstep;
;             PG8_LDB(B0, 0, 0); PG8_LDB(B1, 0, 1); PG8_SCHED; PG8_LDA(At, 0, 0); PG8_STAGE(PG8_SA(1, 1), a1 + hstepA, vc1);
;             if (GA && last && has_next) { const u32x4 q = *gslot; vc0[0] = q.x; vc0[1] = q.y; vc1[0] = q.z; vc1[1] = q.w; }
;             PG8_WAIT_V(8); PG8_WAIT_L(0); PG8_BAR; PG8_MMA(0, 0, At, B0); PG8_MMA(0, 1, At, B1); PG8_BAR; PG8_SCHED;
;             PG8_LDA(At, 0, 1); PG8_STAGE(PG8_SB(0, 0), b2, voffB); PG8_STAGE(PG8_SB(0, 1), b2 + hstep, voffB); PG8_STAGE(PG8_SA(0, 0), a2, vc0);
;             PG8_WAIT_V(8); PG8_WAIT_L(0); PG8_BAR; PG8_MMA(1, 0, At, B0); PG8_MMA(1, 1, At, B1); PG8_BAR; PG8_SCHED;
.LBB0_224:
	ds_read_b128 v[128:131], v139
	ds_read_b128 v[152:155], v139 offset:1024
	ds_read_b128 v[156:159], v139 offset:2048
	ds_read_b128 v[160:163], v139 offset:3072
	ds_read_b128 v[170:173], v164
	ds_read_b128 v[174:177], v164 offset:1024
	ds_read_b128 v[178:181], v164 offset:2048
	ds_read_b128 v[182:185], v164 offset:3072
	s_add_i32 s33, s26, 2
	s_cmp_eq_u32 s55, s26
	s_cselect_b32 s30, s22, s60
	s_cselect_b32 s31, s23, s61
	s_cselect_b32 s28, s24, s62
	s_cselect_b32 s29, s25, s63
	s_add_u32 s26, s30, 0x80
	s_addc_u32 s27, s31, 0
	ds_read_b128 v[186:189], v165
	ds_read_b128 v[190:193], v165 offset:1024
	ds_read_b128 v[194:197], v165 offset:2048
	ds_read_b128 v[198:201], v165 offset:3072
	ds_read_b128 v[202:205], v165 offset:4096
	ds_read_b128 v[206:209], v165 offset:5120
	ds_read_b128 v[210:213], v165 offset:6144
	ds_read_b128 v[218:221], v165 offset:7168
	s_mov_b32 m0, s64
	s_nop 0
	global_load_lds_dwordx4 v132, s[4:5]
	s_mov_b32 m0, s65
	s_nop 0
	global_load_lds_dwordx4 v136, s[4:5]
	s_waitcnt vmcnt(8)
	s_waitcnt lgkmcnt(0)
	s_barrier
	s_setprio 1
	s_waitcnt lgkmcnt(7)
	v_mfma_f32_16x16x32_bf16 v[124:127], v[128:131], v[186:189], v[124:127]
	v_mfma_f32_16x16x32_bf16 v[120:123], v[156:159], v[186:189], v[120:123]
	s_waitcnt lgkmcnt(5)
	v_mfma_f32_16x16x32_bf16 v[108:111], v[128:131], v[194:197], v[108:111]
	v_mfma_f32_16x16x32_bf16 v[104:107], v[156:159], v[194:197], v[104:107]
	s_waitcnt lgkmcnt(3)
	v_mfma_f32_16x16x32_bf16 v[92:95], v[128:131], v[202:205], v[92:95]
	v_mfma_f32_16x16x32_bf16 v[88:91], v[156:159], v[202:205], v[88:91]
	s_waitcnt lgkmcnt(1)
	v_mfma_f32_16x16x32_bf16 v[76:79], v[128:131], v[210:213], v[76:79]
	v_mfma_f32_16x16x32_bf16 v[72:75], v[156:159], v[210:213], v[72:75]
	v_mfma_f32_16x16x32_bf16 v[124:127], v[152:155], v[190:193], v[124:127]
	v_mfma_f32_16x16x32_bf16 v[120:123], v[160:163], v[190:193], v[120:123]
	v_mfma_f32_16x16x32_bf16 v[108:111], v[152:155], v[198:201], v[108:111]
	v_mfma_f32_16x16x32_bf16 v[104:107], v[160:163], v[198:201], v[104:107]
	v_mfma_f32_16x16x32_bf16 v[92:95], v[152:155], v[206:209], v[92:95]
	v_mfma_f32_16x16x32_bf16 v[88:91], v[160:163], v[206:209], v[88:91]
	s_waitcnt lgkmcnt(0)
	v_mfma_f32_16x16x32_bf16 v[76:79], v[152:155], v[218:221], v[76:79]
	v_mfma_f32_16x16x32_bf16 v[72:75], v[160:163], v[218:221], v[72:75]
	s_setprio 0
	s_setprio 1
	v_mfma_f32_16x16x32_bf16 v[116:119], v[170:173], v[186:189], v[116:119]
	v_mfma_f32_16x16x32_bf16 v[112:115], v[178:181], v[186:189], v[112:115]
	v_mfma_f32_16x16x32_bf16 v[100:103], v[170:173], v[194:197], v[100:103]
	v_mfma_f32_16x16x32_bf16 v[96:99], v[178:181], v[194:197], v[96:99]
	v_mfma_f32_16x16x32_bf16 v[84:87], v[170:173], v[202:205], v[84:87]
	v_mfma_f32_16x16x32_bf16 v[80:83], v[178:181], v[202:205], v[80:83]
	v_mfma_f32_16x16x32_bf16 v[68:71], v[170:173], v[210:213], v[68:71]
	v_mfma_f32_16x16x32_bf16 v[64:67], v[178:181], v[210:213], v[64:67]
	v_mfma_f32_16x16x32_bf16 v[116:119], v[174:177], v[190:193], v[116:119]
	v_mfma_f32_16x16x32_bf16 v[112:115], v[182:185], v[190:193], v[112:115]
	v_mfma_f32_16x16x32_bf16 v[100:103], v[174:177], v[198:201], v[100:103]
	v_mfma_f32_16x16x32_bf16 v[96:99], v[182:185], v[198:201], v[96:99]
	v_mfma_f32_16x16x32_bf16 v[84:87], v[174:177], v[206:209], v[84:87]
	v_mfma_f32_16x16x32_bf16 v[80:83], v[182:185], v[206:209], v[80:83]
	v_mfma_f32_16x16x32_bf16 v[68:71], v[174:177], v[218:221], v[68:71]
	v_mfma_f32_16x16x32_bf16 v[64:67], v[182:185], v[218:221], v[64:67]
	s_setprio 0
	s_barrier
	ds_read_b128 v[186:189], v165 offset:16384
	ds_read_b128 v[190:193], v165 offset:17408
	ds_read_b128 v[194:197], v165 offset:18432
	ds_read_b128 v[198:201], v165 offset:19456
	ds_read_b128 v[202:205], v165 offset:20480
	ds_read_b128 v[206:209], v165 offset:21504
	ds_read_b128 v[210:213], v165 offset:22528
	ds_read_b128 v[218:221], v165 offset:23552
	s_mov_b32 m0, s39
	s_nop 0
	global_load_lds_dwordx4 v134, s[28:29]
	s_mov_b32 m0, s40
	s_nop 0
	global_load_lds_dwordx4 v138, s[28:29]
	s_add_u32 s58, s28, s6
	s_addc_u32 s59, s29, s7
	s_mov_b32 m0, s41
	s_nop 0
	global_load_lds_dwordx4 v134, s[58:59]
	s_mov_b32 m0, s42
	s_nop 0
	global_load_lds_dwordx4 v138, s[58:59]
	s_mov_b32 m0, s34
	s_nop 0
	global_load_lds_dwordx4 v132, s[30:31]
	s_mov_b32 m0, s43
	s_nop 0
	global_load_lds_dwordx4 v136, s[30:31]
	s_waitcnt vmcnt(8)
	s_waitcnt lgkmcnt(0)
	s_barrier
	s_setprio 1
	s_waitcnt lgkmcnt(7)
	v_mfma_f32_16x16x32_bf16 v[60:63], v[128:131], v[186:189], v[60:63]
	v_mfma_f32_16x16x32_bf16 v[56:59], v[156:159], v[186:189], v[56:59]
	s_waitcnt lgkmcnt(5)
	v_mfma_f32_16x16x32_bf16 v[44:47], v[128:131], v[194:197], v[44:47]
	v_mfma_f32_16x16x32_bf16 v[40:43], v[156:159], v[194:197], v[40:43]
	s_waitcnt lgkmcnt(3)
	v_mfma_f32_16x16x32_bf16 v[28:31], v[128:131], v[202:205], v[28:31]
	v_mfma_f32_16x16x32_bf16 v[24:27], v[156:159], v[202:205], v[24:27]
	s_waitcnt lgkmcnt(1)
	v_mfma_f32_16x16x32_bf16 v[12:15], v[128:131], v[210:213], v[12:15]
	v_mfma_f32_16x16x32_bf16 v[8:11], v[156:159], v[210:213], v[8:11]
	v_mfma_f32_16x16x32_bf16 v[60:63], v[152:155], v[190:193], v[60:63]
	v_mfma_f32_16x16x32_bf16 v[56:59], v[160:163], v[190:193], v[56:59]
	v_mfma_f32_16x16x32_bf16 v[44:47], v[152:155], v[198:201], v[44:47]
	v_mfma_f32_16x16x32_bf16 v[40:43], v[160:163], v[198:201], v[40:43]
	v_mfma_f32_16x16x32_bf16 v[28:31], v[152:155], v[206:209], v[28:31]
	v_mfma_f32_16x16x32_bf16 v[24:27], v[160:163], v[206:209], v[24:27]
	s_waitcnt lgkmcnt(0)
	v_mfma_f32_16x16x32_bf16 v[12:15], v[152:155], v[218:221], v[12:15]
	v_mfma_f32_16x16x32_bf16 v[8:11], v[160:163], v[218:221], v[8:11]
	s_setprio 0
	s_setprio 1
	v_mfma_f32_16x16x32_bf16 v[52:55], v[170:173], v[186:189], v[52:55]
	v_mfma_f32_16x16x32_bf16 v[48:51], v[178:181], v[186:189], v[48:51]
	v_mfma_f32_16x16x32_bf16 v[36:39], v[170:173], v[194:197], v[36:39]
	v_mfma_f32_16x16x32_bf16 v[32:35], v[178:181], v[194:197], v[32:35]
	v_mfma_f32_16x16x32_bf16 v[20:23], v[170:173], v[202:205], v[20:23]
	v_mfma_f32_16x16x32_bf16 v[16:19], v[178:181], v[202:205], v[16:19]
	v_mfma_f32_16x16x32_bf16 v[4:7], v[170:173], v[210:213], v[4:7]
	v_mfma_f32_16x16x32_bf16 v[0:3], v[178:181], v[210:213], v[0:3]
	v_mfma_f32_16x16x32_bf16 v[52:55], v[174:177], v[190:193], v[52:55]
	v_mfma_f32_16x16x32_bf16 v[48:51], v[182:185], v[190:193], v[48:51]
	v_mfma_f32_16x16x32_bf16 v[36:39], v[174:177], v[198:201], v[36:39]
	v_mfma_f32_16x16x32_bf16 v[32:35], v[182:185], v[198:201], v[32:35]
	v_mfma_f32_16x16x32_bf16 v[20:23], v[174:177], v[206:209], v[20:23]
	v_mfma_f32_16x16x32_bf16 v[16:19], v[182:185], v[206:209], v[16:19]
	v_mfma_f32_16x16x32_bf16 v[4:7], v[174:177], v[218:221], v[4:7]
	v_mfma_f32_16x16x32_bf16 v[0:3], v[182:185], v[218:221], v[0:3]
	s_setprio 0
	s_barrier
; #define PG8_STAGE(bufoff, gbase, voff) do { _Pragma("unroll") for (int _i = 0; _i < 2; ++_i) { unsigned keep_; \
;         asm volatile("s_mov_b32 %0, m0\n\ts_mov_b32 m0, %3\n\ts_nop 0\n\tglobal_load_lds_dwordx4 %1, %2\n\ts_mov_b32 m0, %0" : "=&s"(keep_) : "v"((voff)[_i]), "s"((const char*)(gbase)), "s"(ldsb + (unsigned)((bufoff) + _i * 8192)) : "memory"); } } while (0)
; #define PG8_LDA(dst, b, h) do { _Pragma("unroll") for (int m = 0; m < 4; ++m) _Pragma("unroll") for (int k = 0; k < 2; ++k) dst[m][k] = *(const PG8_LAS bf16x8*)(lds + PG8_SA(b, h) + aoff + m * 2048 + k * 1024); } while (0)
; #define PG8_LDB(dst, b, h) do { _Pragma("unroll") for (int n = 0; n < 2; ++n) _Pragma("unroll") for (int k = 0; k < 2; ++k) dst[n][k] = *(const PG8_LAS bf16x8*)(lds + PG8_SB(b, h) + boff + n * 2048 + k * 1024); } while (0)
; #define PG8_WAIT_V(n) asm volatile("s_waitcnt vmcnt(" #n ")" ::: "memory")
; #define PG8_WAIT_L(n) asm volatile("s_waitcnt lgkmcnt(" #n ")" ::: "memory")
; #define PG8_BAR __builtin_amdgcn_s_barrier()
; #define PG8_SCHED __builtin_amdgcn_sched_barrier(0)
; template <class Epi, class Sched, bool ALIGN_EPI, bool FP8 = false>
; __device__ __forceinline__ void gemm_phase(PG8_LAS unsigned char* lds, const Gemm g, const Sched& S, const Epi& E, const int wid, const int lane) {
;     ...
;             PG8_LDB(B0, 1, 0); PG8_LDB(B1, 1, 1); PG8_SCHED; PG8_LDA(At, 1, 0); PG8_STAGE(PG8_SA(0, 1), a2 + hstepA, vc1);
;             PG8_WAIT_V(8); PG8_WAIT_L(0); PG8_BAR; PG8_MMA(0, 0, At, B0); PG8_MMA(0, 1, At, B1); PG8_BAR; PG8_SCHED;
;             PG8_LDA(At, 1, 1); PG8_STAGE(PG8_SB(1, 0), b3, voffB); PG8_STAGE(PG8_SB(1, 1), b3 + hstep, voffB); PG8_STAGE(PG8_SA(1, 0), a3, vc0);
;             PG8_WAIT_V(8); PG8_WAIT_L(0); PG8_BAR; PG8_MMA(1, 0, At, B0); PG8_MMA(1, 1, At, B1); PG8_BAR; PG8_SCHED;
;         }
	ds_read_b128 v[128:131], v166
	ds_read_b128 v[152:155], v166 offset:1024
	ds_read_b128 v[156:159], v166 offset:2048
	ds_read_b128 v[160:163], v166 offset:3072
	ds_read_b128 v[170:173], v167
	ds_read_b128 v[174:177], v167 offset:1024
	ds_read_b128 v[178:181], v167 offset:2048
	ds_read_b128 v[182:185], v167 offset:3072
	ds_read_b128 v[186:189], v165 offset:32768
	ds_read_b128 v[190:193], v165 offset:33792
	ds_read_b128 v[194:197], v165 offset:34816
	ds_read_b128 v[198:201], v165 offset:35840
	ds_read_b128 v[202:205], v165 offset:36864
	ds_read_b128 v[206:209], v165 offset:37888
	ds_read_b128 v[210:213], v165 offset:38912
	ds_read_b128 v[218:221], v165 offset:39936
	s_add_u32 s30, s30, s6
	s_addc_u32 s31, s31, s7
	s_mov_b32 m0, s44
	s_nop 0
	global_load_lds_dwordx4 v132, s[30:31]
	s_mov_b32 m0, s45
	s_nop 0
	global_load_lds_dwordx4 v136, s[30:31]
	s_waitcnt vmcnt(8)
	s_waitcnt lgkmcnt(0)
	s_barrier
	s_setprio 1
	s_waitcnt lgkmcnt(7)
	v_mfma_f32_16x16x32_bf16 v[124:127], v[128:131], v[186:189], v[124:127]
	v_mfma_f32_16x16x32_bf16 v[120:123], v[156:159], v[186:189], v[120:123]
	s_waitcnt lgkmcnt(5)
	v_mfma_f32_16x16x32_bf16 v[108:111], v[128:131], v[194:197], v[108:111]
	v_mfma_f32_16x16x32_bf16 v[104:107], v[156:159], v[194:197], v[104:107]
	s_waitcnt lgkmcnt(3)
	v_mfma_f32_16x16x32_bf16 v[92:95], v[128:131], v[202:205], v[92:95]
	v_mfma_f32_16x16x32_bf16 v[88:91], v[156:159], v[202:205], v[88:91]
	s_waitcnt lgkmcnt(1)
	v_mfma_f32_16x16x32_bf16 v[76:79], v[128:131], v[210:213], v[76:79]
	v_mfma_f32_16x16x32_bf16 v[72:75], v[156:159], v[210:213], v[72:75]
	v_mfma_f32_16x16x32_bf16 v[124:127], v[152:155], v[190:193], v[124:127]
	v_mfma_f32_16x16x32_bf16 v[120:123], v[160:163], v[190:193], v[120:123]
	v_mfma_f32_16x16x32_bf16 v[108:111], v[152:155], v[198:201], v[108:111]
	v_mfma_f32_16x16x32_bf16 v[104:107], v[160:163], v[198:201], v[104:107]
	v_mfma_f32_16x16x32_bf16 v[92:95], v[152:155], v[206:209], v[92:95]
	v_mfma_f32_16x16x32_bf16 v[88:91], v[160:163], v[206:209], v[88:91]
	s_waitcnt lgkmcnt(0)
	v_mfma_f32_16x16x32_bf16 v[76:79], v[152:155], v[218:221], v[76:79]
	v_mfma_f32_16x16x32_bf16 v[72:75], v[160:163], v[218:221], v[72:75]
	s_setprio 0
	s_setprio 1
	v_mfma_f32_16x16x32_bf16 v[116:119], v[170:173], v[186:189], v[116:119]
	v_mfma_f32_16x16x32_bf16 v[112:115], v[178:181], v[186:189], v[112:115]
	v_mfma_f32_16x16x32_bf16 v[100:103], v[170:173], v[194:197], v[100:103]
	v_mfma_f32_16x16x32_bf16 v[96:99], v[178:181], v[194:197], v[96:99]
	v_mfma_f32_16x16x32_bf16 v[84:87], v[170:173], v[202:205], v[84:87]
	v_mfma_f32_16x16x32_bf16 v[80:83], v[178:181], v[202:205], v[80:83]
	v_mfma_f32_16x16x32_bf16 v[68:71], v[170:173], v[210:213], v[68:71]
	v_mfma_f32_16x16x32_bf16 v[64:67], v[178:181], v[210:213], v[64:67]
	v_mfma_f32_16x16x32_bf16 v[116:119], v[174:177], v[190:193], v[116:119]
	v_mfma_f32_16x16x32_bf16 v[112:115], v[182:185], v[190:193], v[112:115]
	v_mfma_f32_16x16x32_bf16 v[100:103], v[174:177], v[198:201], v[100:103]
	v_mfma_f32_16x16x32_bf16 v[96:99], v[182:185], v[198:201], v[96:99]
	v_mfma_f32_16x16x32_bf16 v[84:87], v[174:177], v[206:209], v[84:87]
	v_mfma_f32_16x16x32_bf16 v[80:83], v[182:185], v[206:209], v[80:83]
	v_mfma_f32_16x16x32_bf16 v[68:71], v[174:177], v[218:221], v[68:71]
	v_mfma_f32_16x16x32_bf16 v[64:67], v[182:185], v[218:221], v[64:67]
	s_setprio 0
	s_barrier
	ds_read_b128 v[186:189], v165 offset:49152
	ds_read_b128 v[190:193], v165 offset:50176
	ds_read_b128 v[194:197], v165 offset:51200
	ds_read_b128 v[198:201], v165 offset:52224
	ds_read_b128 v[202:205], v165 offset:53248
	ds_read_b128 v[206:209], v165 offset:54272
	ds_read_b128 v[210:213], v165 offset:55296
	ds_read_b128 v[218:221], v165 offset:56320
	s_add_u32 s28, s28, 0x80
	s_addc_u32 s29, s29, 0
	s_mov_b32 m0, s49
	s_nop 0
	global_load_lds_dwordx4 v134, s[28:29]
	s_mov_b32 m0, s50
	s_nop 0
	global_load_lds_dwordx4 v138, s[28:29]
	s_add_u32 s28, s28, s6
	s_addc_u32 s29, s29, s7
	s_mov_b32 m0, s53
	s_nop 0
	global_load_lds_dwordx4 v134, s[28:29]
	s_mov_b32 m0, s54
	s_nop 0
	global_load_lds_dwordx4 v138, s[28:29]
	s_mov_b32 m0, s51
	s_nop 0
	global_load_lds_dwordx4 v132, s[26:27]
	s_mov_b32 m0, s52
	s_nop 0
	global_load_lds_dwordx4 v136, s[26:27]
	s_waitcnt vmcnt(8)
	s_waitcnt lgkmcnt(0)
	s_barrier
	s_setprio 1
	s_waitcnt lgkmcnt(7)
	v_mfma_f32_16x16x32_bf16 v[60:63], v[128:131], v[186:189], v[60:63]
	v_mfma_f32_16x16x32_bf16 v[56:59], v[156:159], v[186:189], v[56:59]
	s_waitcnt lgkmcnt(5)
	v_mfma_f32_16x16x32_bf16 v[44:47], v[128:131], v[194:197], v[44:47]
	v_mfma_f32_16x16x32_bf16 v[40:43], v[156:159], v[194:197], v[40:43]
	s_waitcnt lgkmcnt(3)
	v_mfma_f32_16x16x32_bf16 v[28:31], v[128:131], v[202:205], v[28:31]
	v_mfma_f32_16x16x32_bf16 v[24:27], v[156:159], v[202:205], v[24:27]
	s_waitcnt lgkmcnt(1)
	v_mfma_f32_16x16x32_bf16 v[12:15], v[128:131], v[210:213], v[12:15]
	v_mfma_f32_16x16x32_bf16 v[8:11], v[156:159], v[210:213], v[8:11]
	v_mfma_f32_16x16x32_bf16 v[60:63], v[152:155], v[190:193], v[60:63]
	v_mfma_f32_16x16x32_bf16 v[56:59], v[160:163], v[190:193], v[56:59]
	v_mfma_f32_16x16x32_bf16 v[44:47], v[152:155], v[198:201], v[44:47]
	v_mfma_f32_16x16x32_bf16 v[40:43], v[160:163], v[198:201], v[40:43]
	v_mfma_f32_16x16x32_bf16 v[28:31], v[152:155], v[206:209], v[28:31]
	v_mfma_f32_16x16x32_bf16 v[24:27], v[160:163], v[206:209], v[24:27]
	s_waitcnt lgkmcnt(0)
	v_mfma_f32_16x16x32_bf16 v[12:15], v[152:155], v[218:221], v[12:15]
	v_mfma_f32_16x16x32_bf16 v[8:11], v[160:163], v[218:221], v[8:11]
	s_setprio 0
	s_setprio 1
	v_mfma_f32_16x16x32_bf16 v[52:55], v[170:173], v[186:189], v[52:55]
	v_mfma_f32_16x16x32_bf16 v[48:51], v[178:181], v[186:189], v[48:51]
	v_mfma_f32_16x16x32_bf16 v[36:39], v[170:173], v[194:197], v[36:39]
	v_mfma_f32_16x16x32_bf16 v[32:35], v[178:181], v[194:197], v[32:35]
	v_mfma_f32_16x16x32_bf16 v[20:23], v[170:173], v[202:205], v[20:23]
	v_mfma_f32_16x16x32_bf16 v[16:19], v[178:181], v[202:205], v[16:19]
	v_mfma_f32_16x16x32_bf16 v[4:7], v[170:173], v[210:213], v[4:7]
	v_mfma_f32_16x16x32_bf16 v[0:3], v[178:181], v[210:213], v[0:3]
	v_mfma_f32_16x16x32_bf16 v[52:55], v[174:177], v[190:193], v[52:55]
	v_mfma_f32_16x16x32_bf16 v[48:51], v[182:185], v[190:193], v[48:51]
	v_mfma_f32_16x16x32_bf16 v[36:39], v[174:177], v[198:201], v[36:39]
	v_mfma_f32_16x16x32_bf16 v[32:35], v[182:185], v[198:201], v[32:35]
	v_mfma_f32_16x16x32_bf16 v[20:23], v[174:177], v[206:209], v[20:23]
	v_mfma_f32_16x16x32_bf16 v[16:19], v[182:185], v[206:209], v[16:19]
	v_mfma_f32_16x16x32_bf16 v[4:7], v[174:177], v[218:221], v[4:7]
	v_mfma_f32_16x16x32_bf16 v[0:3], v[182:185], v[218:221], v[0:3]
	s_add_u32 s60, s60, 0x100
	s_addc_u32 s61, s61, 0
	s_add_u32 s62, s62, 0x100
	s_addc_u32 s63, s63, 0
	s_add_u32 s4, s4, 0x100
	s_addc_u32 s5, s5, 0
	s_cmp_ge_i32 s33, s46
	s_mov_b32 s26, s33
	s_setprio 0
	s_barrier
	s_cbranch_scc0 .LBB0_224

; #define PG8_STAGE(bufoff, gbase, voff) do { _Pragma("unroll") for (int _i = 0; _i < 2; ++_i) { unsigned keep_; \
;         asm volatile("s_mov_b32 %0, m0\n\ts_mov_b32 m0, %3\n\ts_nop 0\n\tglobal_load_lds_dwordx4 %1, %2\n\ts_mov_b32 m0, %0" : "=&s"(keep_) : "v"((voff)[_i]), "s"((const char*)(gbase)), "s"(ldsb + (unsigned)((bufoff) + _i * 8192)) : "memory"); } } while (0)
; #define PG8_LDA(dst, b, h) do { _Pragma("unroll") for (int m = 0; m < 4; ++m) _Pragma("unroll") for (int k = 0; k < 2; ++k) dst[m][k] = *(const PG8_LAS bf16x8*)(lds + PG8_SA(b, h) + aoff + m * 2048 + k * 1024); } while (0)
; #define PG8_LDB(dst, b, h) do { _Pragma("unroll") for (int n = 0; n < 2; ++n) _Pragma("unroll") for (int k = 0; k < 2; ++k) dst[n][k] = *(const PG8_LAS bf16x8*)(lds + PG8_SB(b, h) + boff + n * 2048 + k * 1024); } while (0)
; #define PG8_WAIT_V(n) asm volatile("s_waitcnt vmcnt(" #n ")" ::: "memory")
; #define PG8_WAIT_L(n) asm volatile("s_waitcnt lgkmcnt(" #n ")" ::: "memory")
; #define PG8_BAR __builtin_amdgcn_s_barrier()
; #define PG8_SCHED __builtin_amdgcn_sched_barrier(0)
; template <class Epi, class Sched, bool ALIGN_EPI, bool FP8 = false>
; __device__ __forceinline__ void gemm_phase(PG8_LAS unsigned char* lds, const Gemm g, const Sched& S, const Epi& E, const int wid, const int lane) {
;     ...
;         for (int t = 0; t < nt; t += 2) {
;             const bool last = (t == nt - 2);
;             const char* a1 = cA + (size_t)(t + 1) * kstep;
;             const char* a2 = last ? nA : cA + (size_t)(t + 2) * kstep; const char* b2 = last ? nB : cB + (size_t)(t + 2) * kstep;
;             const char* a3 = a2 + kstep; const char* b3 = b2 + kstep;
;             PG8_LDB(B0, 0, 0); PG8_LDB(B1, 0, 1); PG8_SCHED; PG8_LDA(At, 0, 0); PG8_STAGE(PG8_SA(1, 1), a1 + hstepA, vc1);
;             if (GA && last && has_next) { const u32x4 q = *gslot; vc0[0] = q.x; vc0[1] = q.y; vc1[0] = q.z; vc1[1] = q.w; }
;             PG8_WAIT_V(8); PG8_WAIT_L(0); PG8_BAR; PG8_MMA(0, 0, At, B0); PG8_MMA(0, 1, At, B1); PG8_BAR; PG8_SCHED;
;             PG8_LDA(At, 0, 1); PG8_STAGE(PG8_SB(0, 0), b2, voffB); PG8_STAGE(PG8_SB(0, 1), b2 + hstep, voffB); PG8_STAGE(PG8_SA(0, 0), a2, vc0);
;             PG8_WAIT_V(8); PG8_WAIT_L(0); PG8_BAR; PG8_MMA(1, 0, At, B0); PG8_MMA(1, 1, At, B1); PG8_BAR; PG8_SCHED;
.LBB0_544:
	ds_read_b128 v[24:27], v165
	ds_read_b128 v[28:31], v165 offset:1024
	ds_read_b128 v[16:19], v165 offset:2048
	ds_read_b128 v[20:23], v165 offset:3072
	ds_read_b128 v[8:11], v167
	ds_read_b128 v[12:15], v167 offset:1024
	ds_read_b128 v[0:3], v167 offset:2048
	ds_read_b128 v[4:7], v167 offset:3072
	s_add_i32 s33, s30, 2
	s_cmp_eq_u32 s66, s30
	s_cselect_b32 s36, s4, s82
	s_cselect_b32 s37, s5, s85
	s_cselect_b32 s34, s26, s86
	s_cselect_b32 s35, s27, s87
	s_add_u32 s30, s36, 0x80
	s_addc_u32 s31, s37, 0
	ds_read_b128 v[178:181], v173
	ds_read_b128 v[182:185], v173 offset:1024
	ds_read_b128 v[186:189], v173 offset:2048
	ds_read_b128 v[190:193], v173 offset:3072
	ds_read_b128 v[194:197], v173 offset:4096
	ds_read_b128 v[198:201], v173 offset:5120
	ds_read_b128 v[202:205], v173 offset:6144
	ds_read_b128 v[206:209], v173 offset:7168
	s_mov_b32 m0, s67
	s_nop 0
	global_load_lds_dwordx4 v160, s[28:29]
	s_mov_b32 m0, s68
	s_nop 0
	global_load_lds_dwordx4 v164, s[28:29]
	s_waitcnt vmcnt(8)
	s_waitcnt lgkmcnt(0)
	s_barrier
	s_setprio 1
	s_waitcnt lgkmcnt(6)
	v_mfma_scale_f32_16x16x128_f8f6f4 v[156:159], v[24:31], v[178:185], v[156:159], v174, v175 op_sel_hi:[0,0,0]
	v_mfma_scale_f32_16x16x128_f8f6f4 v[152:155], v[16:23], v[178:185], v[152:155], v174, v175 op_sel_hi:[0,0,0]
	s_waitcnt lgkmcnt(4)
	v_mfma_scale_f32_16x16x128_f8f6f4 v[140:143], v[24:31], v[186:193], v[140:143], v174, v175 op_sel_hi:[0,0,0]
	v_mfma_scale_f32_16x16x128_f8f6f4 v[136:139], v[16:23], v[186:193], v[136:139], v174, v175 op_sel_hi:[0,0,0]
	s_waitcnt lgkmcnt(2)
	v_mfma_scale_f32_16x16x128_f8f6f4 v[124:127], v[24:31], v[194:201], v[124:127], v174, v175 op_sel_hi:[0,0,0]
	v_mfma_scale_f32_16x16x128_f8f6f4 v[120:123], v[16:23], v[194:201], v[120:123], v174, v175 op_sel_hi:[0,0,0]
	s_waitcnt lgkmcnt(0)
	v_mfma_scale_f32_16x16x128_f8f6f4 v[108:111], v[24:31], v[202:209], v[108:111], v174, v175 op_sel_hi:[0,0,0]
	v_mfma_scale_f32_16x16x128_f8f6f4 v[104:107], v[16:23], v[202:209], v[104:107], v174, v175 op_sel_hi:[0,0,0]
	s_setprio 0
	s_setprio 1
	v_mfma_scale_f32_16x16x128_f8f6f4 v[148:151], v[8:15], v[178:185], v[148:151], v174, v175 op_sel_hi:[0,0,0]
	v_mfma_scale_f32_16x16x128_f8f6f4 v[144:147], v[0:7], v[178:185], v[144:147], v174, v175 op_sel_hi:[0,0,0]
	v_mfma_scale_f32_16x16x128_f8f6f4 v[132:135], v[8:15], v[186:193], v[132:135], v174, v175 op_sel_hi:[0,0,0]
	v_mfma_scale_f32_16x16x128_f8f6f4 v[128:131], v[0:7], v[186:193], v[128:131], v174, v175 op_sel_hi:[0,0,0]
	v_mfma_scale_f32_16x16x128_f8f6f4 v[116:119], v[8:15], v[194:201], v[116:119], v174, v175 op_sel_hi:[0,0,0]
	v_mfma_scale_f32_16x16x128_f8f6f4 v[112:115], v[0:7], v[194:201], v[112:115], v174, v175 op_sel_hi:[0,0,0]
	v_mfma_scale_f32_16x16x128_f8f6f4 v[100:103], v[8:15], v[202:209], v[100:103], v174, v175 op_sel_hi:[0,0,0]
	v_mfma_scale_f32_16x16x128_f8f6f4 v[96:99], v[0:7], v[202:209], v[96:99], v174, v175 op_sel_hi:[0,0,0]
	s_setprio 0
	s_barrier
	ds_read_b128 v[178:181], v173 offset:16384
	ds_read_b128 v[182:185], v173 offset:17408
	ds_read_b128 v[186:189], v173 offset:18432
	ds_read_b128 v[190:193], v173 offset:19456
	ds_read_b128 v[194:197], v173 offset:20480
	ds_read_b128 v[198:201], v173 offset:21504
	ds_read_b128 v[202:205], v173 offset:22528
	ds_read_b128 v[206:209], v173 offset:23552
	s_mov_b32 m0, s44
	s_nop 0
	global_load_lds_dwordx4 v162, s[34:35]
	s_mov_b32 m0, s45
	s_nop 0
	global_load_lds_dwordx4 v166, s[34:35]
	s_add_u32 s58, s34, s6
	s_addc_u32 s59, s35, s7
	s_mov_b32 m0, s46
	s_nop 0
	global_load_lds_dwordx4 v162, s[58:59]
	s_mov_b32 m0, s47
	s_nop 0
	global_load_lds_dwordx4 v166, s[58:59]
	s_mov_b32 m0, s42
	s_nop 0
	global_load_lds_dwordx4 v160, s[36:37]
	s_mov_b32 m0, s48
	s_nop 0
	global_load_lds_dwordx4 v164, s[36:37]
	s_waitcnt vmcnt(8)
	s_waitcnt lgkmcnt(0)
	s_barrier
	s_setprio 1
	s_waitcnt lgkmcnt(6)
	v_mfma_scale_f32_16x16x128_f8f6f4 v[92:95], v[24:31], v[178:185], v[92:95], v174, v175 op_sel_hi:[0,0,0]
	v_mfma_scale_f32_16x16x128_f8f6f4 v[88:91], v[16:23], v[178:185], v[88:91], v174, v175 op_sel_hi:[0,0,0]
	s_waitcnt lgkmcnt(4)
	v_mfma_scale_f32_16x16x128_f8f6f4 v[76:79], v[24:31], v[186:193], v[76:79], v174, v175 op_sel_hi:[0,0,0]
	v_mfma_scale_f32_16x16x128_f8f6f4 v[72:75], v[16:23], v[186:193], v[72:75], v174, v175 op_sel_hi:[0,0,0]
	s_waitcnt lgkmcnt(2)
	v_mfma_scale_f32_16x16x128_f8f6f4 v[60:63], v[24:31], v[194:201], v[60:63], v174, v175 op_sel_hi:[0,0,0]
	v_mfma_scale_f32_16x16x128_f8f6f4 v[56:59], v[16:23], v[194:201], v[56:59], v174, v175 op_sel_hi:[0,0,0]
	s_waitcnt lgkmcnt(0)
	v_mfma_scale_f32_16x16x128_f8f6f4 v[44:47], v[24:31], v[202:209], v[44:47], v174, v175 op_sel_hi:[0,0,0]
	v_mfma_scale_f32_16x16x128_f8f6f4 v[40:43], v[16:23], v[202:209], v[40:43], v174, v175 op_sel_hi:[0,0,0]
	s_setprio 0
	s_setprio 1
	v_mfma_scale_f32_16x16x128_f8f6f4 v[84:87], v[8:15], v[178:185], v[84:87], v174, v175 op_sel_hi:[0,0,0]
	v_mfma_scale_f32_16x16x128_f8f6f4 v[80:83], v[0:7], v[178:185], v[80:83], v174, v175 op_sel_hi:[0,0,0]
	v_mfma_scale_f32_16x16x128_f8f6f4 v[68:71], v[8:15], v[186:193], v[68:71], v174, v175 op_sel_hi:[0,0,0]
	v_mfma_scale_f32_16x16x128_f8f6f4 v[64:67], v[0:7], v[186:193], v[64:67], v174, v175 op_sel_hi:[0,0,0]
	v_mfma_scale_f32_16x16x128_f8f6f4 v[52:55], v[8:15], v[194:201], v[52:55], v174, v175 op_sel_hi:[0,0,0]
	v_mfma_scale_f32_16x16x128_f8f6f4 v[48:51], v[0:7], v[194:201], v[48:51], v174, v175 op_sel_hi:[0,0,0]
	v_mfma_scale_f32_16x16x128_f8f6f4 v[36:39], v[8:15], v[202:209], v[36:39], v174, v175 op_sel_hi:[0,0,0]
	v_mfma_scale_f32_16x16x128_f8f6f4 v[32:35], v[0:7], v[202:209], v[32:35], v174, v175 op_sel_hi:[0,0,0]
	s_setprio 0
	s_barrier
; #define PG8_STAGE(bufoff, gbase, voff) do { _Pragma("unroll") for (int _i = 0; _i < 2; ++_i) { unsigned keep_; \
;         asm volatile("s_mov_b32 %0, m0\n\ts_mov_b32 m0, %3\n\ts_nop 0\n\tglobal_load_lds_dwordx4 %1, %2\n\ts_mov_b32 m0, %0" : "=&s"(keep_) : "v"((voff)[_i]), "s"((const char*)(gbase)), "s"(ldsb + (unsigned)((bufoff) + _i * 8192)) : "memory"); } } while (0)
; #define PG8_LDA(dst, b, h) do { _Pragma("unroll") for (int m = 0; m < 4; ++m) _Pragma("unroll") for (int k = 0; k < 2; ++k) dst[m][k] = *(const PG8_LAS bf16x8*)(lds + PG8_SA(b, h) + aoff + m * 2048 + k * 1024); } while (0)
; #define PG8_LDB(dst, b, h) do { _Pragma("unroll") for (int n = 0; n < 2; ++n) _Pragma("unroll") for (int k = 0; k < 2; ++k) dst[n][k] = *(const PG8_LAS bf16x8*)(lds + PG8_SB(b, h) + boff + n * 2048 + k * 1024); } while (0)
; #define PG8_WAIT_V(n) asm volatile("s_waitcnt vmcnt(" #n ")" ::: "memory")
; #define PG8_WAIT_L(n) asm volatile("s_waitcnt lgkmcnt(" #n ")" ::: "memory")
; #define PG8_BAR __builtin_amdgcn_s_barrier()
; #define PG8_SCHED __builtin_amdgcn_sched_barrier(0)
; template <class Epi, class Sched, bool ALIGN_EPI, bool FP8 = false>
; __device__ __forceinline__ void gemm_phase(PG8_LAS unsigned char* lds, const Gemm g, const Sched& S, const Epi& E, const int wid, const int lane) {
;     ...
;             PG8_LDB(B0, 1, 0); PG8_LDB(B1, 1, 1); PG8_SCHED; PG8_LDA(At, 1, 0); PG8_STAGE(PG8_SA(0, 1), a2 + hstepA, vc1);
;             PG8_WAIT_V(8); PG8_WAIT_L(0); PG8_BAR; PG8_MMA(0, 0, At, B0); PG8_MMA(0, 1, At, B1); PG8_BAR; PG8_SCHED;
;             PG8_LDA(At, 1, 1); PG8_STAGE(PG8_SB(1, 0), b3, voffB); PG8_STAGE(PG8_SB(1, 1), b3 + hstep, voffB); PG8_STAGE(PG8_SA(1, 0), a3, vc0);
;             PG8_WAIT_V(8); PG8_WAIT_L(0); PG8_BAR; PG8_MMA(1, 0, At, B0); PG8_MMA(1, 1, At, B1); PG8_BAR; PG8_SCHED;
;         }
	ds_read_b128 v[0:3], v176
	ds_read_b128 v[4:7], v176 offset:1024
	ds_read_b128 v[8:11], v176 offset:2048
	ds_read_b128 v[12:15], v176 offset:3072
	ds_read_b128 v[16:19], v177
	ds_read_b128 v[20:23], v177 offset:1024
	ds_read_b128 v[24:27], v177 offset:2048
	ds_read_b128 v[28:31], v177 offset:3072
	ds_read_b128 v[178:181], v173 offset:32768
	ds_read_b128 v[182:185], v173 offset:33792
	ds_read_b128 v[186:189], v173 offset:34816
	ds_read_b128 v[190:193], v173 offset:35840
	ds_read_b128 v[194:197], v173 offset:36864
	ds_read_b128 v[198:201], v173 offset:37888
	ds_read_b128 v[202:205], v173 offset:38912
	ds_read_b128 v[206:209], v173 offset:39936
	s_add_u32 s36, s36, s6
	s_addc_u32 s37, s37, s7
	s_mov_b32 m0, s49
	s_nop 0
	global_load_lds_dwordx4 v160, s[36:37]
	s_mov_b32 m0, s50
	s_nop 0
	global_load_lds_dwordx4 v164, s[36:37]
	s_waitcnt vmcnt(8)
	s_waitcnt lgkmcnt(0)
	s_barrier
	s_setprio 1
	s_waitcnt lgkmcnt(6)
	v_mfma_scale_f32_16x16x128_f8f6f4 v[156:159], v[0:7], v[178:185], v[156:159], v174, v175 op_sel_hi:[0,0,0]
	v_mfma_scale_f32_16x16x128_f8f6f4 v[152:155], v[8:15], v[178:185], v[152:155], v174, v175 op_sel_hi:[0,0,0]
	s_waitcnt lgkmcnt(4)
	v_mfma_scale_f32_16x16x128_f8f6f4 v[140:143], v[0:7], v[186:193], v[140:143], v174, v175 op_sel_hi:[0,0,0]
	v_mfma_scale_f32_16x16x128_f8f6f4 v[136:139], v[8:15], v[186:193], v[136:139], v174, v175 op_sel_hi:[0,0,0]
	s_waitcnt lgkmcnt(2)
	v_mfma_scale_f32_16x16x128_f8f6f4 v[124:127], v[0:7], v[194:201], v[124:127], v174, v175 op_sel_hi:[0,0,0]
	v_mfma_scale_f32_16x16x128_f8f6f4 v[120:123], v[8:15], v[194:201], v[120:123], v174, v175 op_sel_hi:[0,0,0]
	s_waitcnt lgkmcnt(0)
	v_mfma_scale_f32_16x16x128_f8f6f4 v[108:111], v[0:7], v[202:209], v[108:111], v174, v175 op_sel_hi:[0,0,0]
	v_mfma_scale_f32_16x16x128_f8f6f4 v[104:107], v[8:15], v[202:209], v[104:107], v174, v175 op_sel_hi:[0,0,0]
	s_setprio 0
	s_setprio 1
	v_mfma_scale_f32_16x16x128_f8f6f4 v[148:151], v[16:23], v[178:185], v[148:151], v174, v175 op_sel_hi:[0,0,0]
	v_mfma_scale_f32_16x16x128_f8f6f4 v[144:147], v[24:31], v[178:185], v[144:147], v174, v175 op_sel_hi:[0,0,0]
	v_mfma_scale_f32_16x16x128_f8f6f4 v[132:135], v[16:23], v[186:193], v[132:135], v174, v175 op_sel_hi:[0,0,0]
	v_mfma_scale_f32_16x16x128_f8f6f4 v[128:131], v[24:31], v[186:193], v[128:131], v174, v175 op_sel_hi:[0,0,0]
	v_mfma_scale_f32_16x16x128_f8f6f4 v[116:119], v[16:23], v[194:201], v[116:119], v174, v175 op_sel_hi:[0,0,0]
	v_mfma_scale_f32_16x16x128_f8f6f4 v[112:115], v[24:31], v[194:201], v[112:115], v174, v175 op_sel_hi:[0,0,0]
	v_mfma_scale_f32_16x16x128_f8f6f4 v[100:103], v[16:23], v[202:209], v[100:103], v174, v175 op_sel_hi:[0,0,0]
	v_mfma_scale_f32_16x16x128_f8f6f4 v[96:99], v[24:31], v[202:209], v[96:99], v174, v175 op_sel_hi:[0,0,0]
	s_setprio 0
	s_barrier
	ds_read_b128 v[178:181], v173 offset:49152
	ds_read_b128 v[182:185], v173 offset:50176
	ds_read_b128 v[186:189], v173 offset:51200
	ds_read_b128 v[190:193], v173 offset:52224
	ds_read_b128 v[194:197], v173 offset:53248
	ds_read_b128 v[198:201], v173 offset:54272
	ds_read_b128 v[202:205], v173 offset:55296
	ds_read_b128 v[206:209], v173 offset:56320
	s_add_u32 s34, s34, 0x80
	s_addc_u32 s35, s35, 0
	s_mov_b32 m0, s52
	s_nop 0
	global_load_lds_dwordx4 v162, s[34:35]
	s_mov_b32 m0, s53
	s_nop 0
	global_load_lds_dwordx4 v166, s[34:35]
	s_add_u32 s34, s34, s6
	s_addc_u32 s35, s35, s7
	s_mov_b32 m0, s64
	s_nop 0
	global_load_lds_dwordx4 v162, s[34:35]
	s_mov_b32 m0, s65
	s_nop 0
	global_load_lds_dwordx4 v166, s[34:35]
	s_mov_b32 m0, s54
	s_nop 0
	global_load_lds_dwordx4 v160, s[30:31]
	s_mov_b32 m0, s55
	s_nop 0
	global_load_lds_dwordx4 v164, s[30:31]
	s_waitcnt vmcnt(8)
	s_waitcnt lgkmcnt(0)
	s_barrier
	s_setprio 1
	s_waitcnt lgkmcnt(6)
	v_mfma_scale_f32_16x16x128_f8f6f4 v[92:95], v[0:7], v[178:185], v[92:95], v174, v175 op_sel_hi:[0,0,0]
	v_mfma_scale_f32_16x16x128_f8f6f4 v[88:91], v[8:15], v[178:185], v[88:91], v174, v175 op_sel_hi:[0,0,0]
	s_waitcnt lgkmcnt(4)
	v_mfma_scale_f32_16x16x128_f8f6f4 v[76:79], v[0:7], v[186:193], v[76:79], v174, v175 op_sel_hi:[0,0,0]
	v_mfma_scale_f32_16x16x128_f8f6f4 v[72:75], v[8:15], v[186:193], v[72:75], v174, v175 op_sel_hi:[0,0,0]
	s_waitcnt lgkmcnt(2)
	v_mfma_scale_f32_16x16x128_f8f6f4 v[60:63], v[0:7], v[194:201], v[60:63], v174, v175 op_sel_hi:[0,0,0]
	v_mfma_scale_f32_16x16x128_f8f6f4 v[56:59], v[8:15], v[194:201], v[56:59], v174, v175 op_sel_hi:[0,0,0]
	s_waitcnt lgkmcnt(0)
	v_mfma_scale_f32_16x16x128_f8f6f4 v[44:47], v[0:7], v[202:209], v[44:47], v174, v175 op_sel_hi:[0,0,0]
	v_mfma_scale_f32_16x16x128_f8f6f4 v[40:43], v[8:15], v[202:209], v[40:43], v174, v175 op_sel_hi:[0,0,0]
	s_setprio 0
	s_setprio 1
	v_mfma_scale_f32_16x16x128_f8f6f4 v[84:87], v[16:23], v[178:185], v[84:87], v174, v175 op_sel_hi:[0,0,0]
	v_mfma_scale_f32_16x16x128_f8f6f4 v[80:83], v[24:31], v[178:185], v[80:83], v174, v175 op_sel_hi:[0,0,0]
	v_mfma_scale_f32_16x16x128_f8f6f4 v[68:71], v[16:23], v[186:193], v[68:71], v174, v175 op_sel_hi:[0,0,0]
	v_mfma_scale_f32_16x16x128_f8f6f4 v[64:67], v[24:31], v[186:193], v[64:67], v174, v175 op_sel_hi:[0,0,0]
	v_mfma_scale_f32_16x16x128_f8f6f4 v[52:55], v[16:23], v[194:201], v[52:55], v174, v175 op_sel_hi:[0,0,0]
	v_mfma_scale_f32_16x16x128_f8f6f4 v[48:51], v[24:31], v[194:201], v[48:51], v174, v175 op_sel_hi:[0,0,0]
	v_mfma_scale_f32_16x16x128_f8f6f4 v[36:39], v[16:23], v[202:209], v[36:39], v174, v175 op_sel_hi:[0,0,0]
	v_mfma_scale_f32_16x16x128_f8f6f4 v[32:35], v[24:31], v[202:209], v[32:35], v174, v175 op_sel_hi:[0,0,0]
	s_add_u32 s82, s82, 0x100
	s_addc_u32 s85, s85, 0
	s_add_u32 s86, s86, 0x100
	s_addc_u32 s87, s87, 0
	s_add_u32 s28, s28, 0x100
	s_addc_u32 s29, s29, 0
	s_cmp_ge_i32 s33, s51
	s_mov_b32 s30, s33
	s_setprio 0
	s_barrier
	s_cbranch_scc0 .LBB0_544

; #define PG8_STAGE(bufoff, gbase, voff) do { _Pragma("unroll") for (int _i = 0; _i < 2; ++_i) { unsigned keep_; \
;         asm volatile("s_mov_b32 %0, m0\n\ts_mov_b32 m0, %3\n\ts_nop 0\n\tglobal_load_lds_dwordx4 %1, %2\n\ts_mov_b32 m0, %0" : "=&s"(keep_) : "v"((voff)[_i]), "s"((const char*)(gbase)), "s"(ldsb + (unsigned)((bufoff) + _i * 8192)) : "memory"); } } while (0)
; #define PG8_LDA(dst, b, h) do { _Pragma("unroll") for (int m = 0; m < 4; ++m) _Pragma("unroll") for (int k = 0; k < 2; ++k) dst[m][k] = *(const PG8_LAS bf16x8*)(lds + PG8_SA(b, h) + aoff + m * 2048 + k * 1024); } while (0)
; #define PG8_LDB(dst, b, h) do { _Pragma("unroll") for (int n = 0; n < 2; ++n) _Pragma("unroll") for (int k = 0; k < 2; ++k) dst[n][k] = *(const PG8_LAS bf16x8*)(lds + PG8_SB(b, h) + boff + n * 2048 + k * 1024); } while (0)
; #define PG8_WAIT_V(n) asm volatile("s_waitcnt vmcnt(" #n ")" ::: "memory")
; #define PG8_WAIT_L(n) asm volatile("s_waitcnt lgkmcnt(" #n ")" ::: "memory")
; #define PG8_BAR __builtin_amdgcn_s_barrier()
; #define PG8_SCHED __builtin_amdgcn_sched_barrier(0)
; template <class Epi, class Sched, bool ALIGN_EPI, bool FP8 = false>
; __device__ __forceinline__ void gemm_phase(PG8_LAS unsigned char* lds, const Gemm g, const Sched& S, const Epi& E, const int wid, const int lane) {
;     ...
;         for (int t = 0; t < nt; t += 2) {
;             const bool last = (t == nt - 2);
;             const char* a1 = cA + (size_t)(t + 1) * kstep;
;             const char* a2 = last ? nA : cA + (size_t)(t + 2) * kstep; const char* b2 = last ? nB : cB + (size_t)(t + 2) * kstep;
;             const char* a3 = a2 + kstep; const char* b3 = b2 + kstep;
;             PG8_LDB(B0, 0, 0); PG8_LDB(B1, 0, 1); PG8_SCHED; PG8_LDA(At, 0, 0); PG8_STAGE(PG8_SA(1, 1), a1 + hstepA, vc1);
;             if (GA && last && has_next) { const u32x4 q = *gslot; vc0[0] = q.x; vc0[1] = q.y; vc1[0] = q.z; vc1[1] = q.w; }
;             PG8_WAIT_V(8); PG8_WAIT_L(0); PG8_BAR; PG8_MMA(0, 0, At, B0); PG8_MMA(0, 1, At, B1); PG8_BAR; PG8_SCHED;
;             PG8_LDA(At, 0, 1); PG8_STAGE(PG8_SB(0, 0), b2, voffB); PG8_STAGE(PG8_SB(0, 1), b2 + hstep, voffB); PG8_STAGE(PG8_SA(0, 0), a2, vc0);
;             PG8_WAIT_V(8); PG8_WAIT_L(0); PG8_BAR; PG8_MMA(1, 0, At, B0); PG8_MMA(1, 1, At, B1); PG8_BAR; PG8_SCHED;
.LBB0_727:
	s_add_i32 s82, s82, 2
	s_and_b64 s[8:9], s[38:39], exec
	s_cselect_b32 s9, 0, s6
	s_cselect_b32 s8, 0, s7
	s_add_u32 s40, s20, s9
	s_addc_u32 s41, s21, s8
	s_add_u32 s33, s34, s6
	s_addc_u32 s42, s35, s7
	s_add_u32 s8, s40, 0x80
	s_addc_u32 s9, s41, 0
	s_waitcnt vmcnt(8)
	s_and_b64 s[38:39], s[38:39], exec
	s_waitcnt lgkmcnt(0)
	s_cselect_b32 s43, s31, s42
	s_cselect_b32 s42, s30, s33
	s_add_u32 s38, s42, 0x80
	s_addc_u32 s39, s43, 0
	s_barrier
	s_setprio 1
	s_waitcnt lgkmcnt(6)
	v_mfma_scale_f32_16x16x128_f8f6f4 v[192:195], v[24:31], v[56:63], v[192:195], v210, v211 op_sel_hi:[0,0,0]
	v_mfma_scale_f32_16x16x128_f8f6f4 v[184:187], v[16:23], v[56:63], v[184:187], v210, v211 op_sel_hi:[0,0,0]
	s_waitcnt lgkmcnt(4)
	v_mfma_scale_f32_16x16x128_f8f6f4 v[176:179], v[24:31], v[48:55], v[176:179], v210, v211 op_sel_hi:[0,0,0]
	v_mfma_scale_f32_16x16x128_f8f6f4 v[168:171], v[16:23], v[48:55], v[168:171], v210, v211 op_sel_hi:[0,0,0]
	s_waitcnt lgkmcnt(2)
	v_mfma_scale_f32_16x16x128_f8f6f4 v[160:163], v[24:31], v[40:47], v[160:163], v210, v211 op_sel_hi:[0,0,0]
	v_mfma_scale_f32_16x16x128_f8f6f4 v[152:155], v[16:23], v[40:47], v[152:155], v210, v211 op_sel_hi:[0,0,0]
	s_waitcnt lgkmcnt(0)
	v_mfma_scale_f32_16x16x128_f8f6f4 v[144:147], v[24:31], v[32:39], v[144:147], v210, v211 op_sel_hi:[0,0,0]
	v_mfma_scale_f32_16x16x128_f8f6f4 v[136:139], v[16:23], v[32:39], v[136:139], v210, v211 op_sel_hi:[0,0,0]
	s_setprio 0
	s_setprio 1
	v_mfma_scale_f32_16x16x128_f8f6f4 v[188:191], v[8:15], v[56:63], v[188:191], v210, v211 op_sel_hi:[0,0,0]
	v_mfma_scale_f32_16x16x128_f8f6f4 v[180:183], v[0:7], v[56:63], v[180:183], v210, v211 op_sel_hi:[0,0,0]
	v_mfma_scale_f32_16x16x128_f8f6f4 v[172:175], v[8:15], v[48:55], v[172:175], v210, v211 op_sel_hi:[0,0,0]
	v_mfma_scale_f32_16x16x128_f8f6f4 v[164:167], v[0:7], v[48:55], v[164:167], v210, v211 op_sel_hi:[0,0,0]
	v_mfma_scale_f32_16x16x128_f8f6f4 v[156:159], v[8:15], v[40:47], v[156:159], v210, v211 op_sel_hi:[0,0,0]
	v_mfma_scale_f32_16x16x128_f8f6f4 v[148:151], v[0:7], v[40:47], v[148:151], v210, v211 op_sel_hi:[0,0,0]
	v_mfma_scale_f32_16x16x128_f8f6f4 v[140:143], v[8:15], v[32:39], v[140:143], v210, v211 op_sel_hi:[0,0,0]
	v_mfma_scale_f32_16x16x128_f8f6f4 v[132:135], v[0:7], v[32:39], v[132:135], v210, v211 op_sel_hi:[0,0,0]
	s_setprio 0
	s_barrier
	ds_read_b128 v[32:35], v209 offset:16384
	ds_read_b128 v[36:39], v209 offset:17408
	ds_read_b128 v[40:43], v209 offset:18432
	ds_read_b128 v[44:47], v209 offset:19456
	ds_read_b128 v[48:51], v209 offset:20480
	ds_read_b128 v[52:55], v209 offset:21504
	ds_read_b128 v[56:59], v209 offset:22528
	ds_read_b128 v[60:63], v209 offset:23552
	s_mov_b32 m0, s51
	s_nop 0
	global_load_lds_dwordx4 v200, s[42:43]
	s_mov_b32 m0, s53
	s_nop 0
	global_load_lds_dwordx4 v202, s[42:43]
	s_add_u32 s42, s42, s16
	s_addc_u32 s43, s43, s17
	s_mov_b32 m0, s55
	s_nop 0
	global_load_lds_dwordx4 v200, s[42:43]
	s_mov_b32 m0, s64
	s_nop 0
	global_load_lds_dwordx4 v202, s[42:43]
	s_mov_b32 m0, s47
	s_nop 0
	global_load_lds_dwordx4 v64, s[40:41]
	s_mov_b32 m0, s65
	s_nop 0
	global_load_lds_dwordx4 v65, s[40:41]
	s_waitcnt vmcnt(8)
	s_waitcnt lgkmcnt(0)
	s_barrier
	s_setprio 1
	s_waitcnt lgkmcnt(6)
	v_mfma_scale_f32_16x16x128_f8f6f4 v[128:131], v[24:31], v[32:39], v[128:131], v210, v211 op_sel_hi:[0,0,0]
	v_mfma_scale_f32_16x16x128_f8f6f4 v[120:123], v[16:23], v[32:39], v[120:123], v210, v211 op_sel_hi:[0,0,0]
	s_waitcnt lgkmcnt(4)
	v_mfma_scale_f32_16x16x128_f8f6f4 v[112:115], v[24:31], v[40:47], v[112:115], v210, v211 op_sel_hi:[0,0,0]
	v_mfma_scale_f32_16x16x128_f8f6f4 v[104:107], v[16:23], v[40:47], v[104:107], v210, v211 op_sel_hi:[0,0,0]
	s_waitcnt lgkmcnt(2)
	v_mfma_scale_f32_16x16x128_f8f6f4 v[96:99], v[24:31], v[48:55], v[96:99], v210, v211 op_sel_hi:[0,0,0]
	v_mfma_scale_f32_16x16x128_f8f6f4 v[88:91], v[16:23], v[48:55], v[88:91], v210, v211 op_sel_hi:[0,0,0]
	s_waitcnt lgkmcnt(0)
	v_mfma_scale_f32_16x16x128_f8f6f4 v[80:83], v[24:31], v[56:63], v[80:83], v210, v211 op_sel_hi:[0,0,0]
	v_mfma_scale_f32_16x16x128_f8f6f4 v[72:75], v[16:23], v[56:63], v[72:75], v210, v211 op_sel_hi:[0,0,0]
	s_setprio 0
	s_setprio 1
	v_mfma_scale_f32_16x16x128_f8f6f4 v[124:127], v[8:15], v[32:39], v[124:127], v210, v211 op_sel_hi:[0,0,0]
	v_mfma_scale_f32_16x16x128_f8f6f4 v[116:119], v[0:7], v[32:39], v[116:119], v210, v211 op_sel_hi:[0,0,0]
	v_mfma_scale_f32_16x16x128_f8f6f4 v[108:111], v[8:15], v[40:47], v[108:111], v210, v211 op_sel_hi:[0,0,0]
	v_mfma_scale_f32_16x16x128_f8f6f4 v[100:103], v[0:7], v[40:47], v[100:103], v210, v211 op_sel_hi:[0,0,0]
	v_mfma_scale_f32_16x16x128_f8f6f4 v[92:95], v[8:15], v[48:55], v[92:95], v210, v211 op_sel_hi:[0,0,0]
	v_mfma_scale_f32_16x16x128_f8f6f4 v[84:87], v[0:7], v[48:55], v[84:87], v210, v211 op_sel_hi:[0,0,0]
	v_mfma_scale_f32_16x16x128_f8f6f4 v[76:79], v[8:15], v[56:63], v[76:79], v210, v211 op_sel_hi:[0,0,0]
	v_mfma_scale_f32_16x16x128_f8f6f4 v[68:71], v[0:7], v[56:63], v[68:71], v210, v211 op_sel_hi:[0,0,0]
	s_setprio 0
	s_barrier
; #define PG8_STAGE(bufoff, gbase, voff) do { _Pragma("unroll") for (int _i = 0; _i < 2; ++_i) { unsigned keep_; \
;         asm volatile("s_mov_b32 %0, m0\n\ts_mov_b32 m0, %3\n\ts_nop 0\n\tglobal_load_lds_dwordx4 %1, %2\n\ts_mov_b32 m0, %0" : "=&s"(keep_) : "v"((voff)[_i]), "s"((const char*)(gbase)), "s"(ldsb + (unsigned)((bufoff) + _i * 8192)) : "memory"); } } while (0)
; #define PG8_LDA(dst, b, h) do { _Pragma("unroll") for (int m = 0; m < 4; ++m) _Pragma("unroll") for (int k = 0; k < 2; ++k) dst[m][k] = *(const PG8_LAS bf16x8*)(lds + PG8_SA(b, h) + aoff + m * 2048 + k * 1024); } while (0)
; #define PG8_LDB(dst, b, h) do { _Pragma("unroll") for (int n = 0; n < 2; ++n) _Pragma("unroll") for (int k = 0; k < 2; ++k) dst[n][k] = *(const PG8_LAS bf16x8*)(lds + PG8_SB(b, h) + boff + n * 2048 + k * 1024); } while (0)
; #define PG8_WAIT_V(n) asm volatile("s_waitcnt vmcnt(" #n ")" ::: "memory")
; #define PG8_WAIT_L(n) asm volatile("s_waitcnt lgkmcnt(" #n ")" ::: "memory")
; #define PG8_BAR __builtin_amdgcn_s_barrier()
; #define PG8_SCHED __builtin_amdgcn_sched_barrier(0)
; template <class Epi, class Sched, bool ALIGN_EPI, bool FP8 = false>
; __device__ __forceinline__ void gemm_phase(PG8_LAS unsigned char* lds, const Gemm g, const Sched& S, const Epi& E, const int wid, const int lane) {
;     ...
;             PG8_LDB(B0, 1, 0); PG8_LDB(B1, 1, 1); PG8_SCHED; PG8_LDA(At, 1, 0); PG8_STAGE(PG8_SA(0, 1), a2 + hstepA, vc1);
;             PG8_WAIT_V(8); PG8_WAIT_L(0); PG8_BAR; PG8_MMA(0, 0, At, B0); PG8_MMA(0, 1, At, B1); PG8_BAR; PG8_SCHED;
;             PG8_LDA(At, 1, 1); PG8_STAGE(PG8_SB(1, 0), b3, voffB); PG8_STAGE(PG8_SB(1, 1), b3 + hstep, voffB); PG8_STAGE(PG8_SA(1, 0), a3, vc0);
;             PG8_WAIT_V(8); PG8_WAIT_L(0); PG8_BAR; PG8_MMA(1, 0, At, B0); PG8_MMA(1, 1, At, B1); PG8_BAR; PG8_SCHED;
;         }
	v_add_u32_e32 v12, 0x18000, v206
	v_add_u32_e32 v28, 0x1c000, v206
	ds_read_b128 v[0:3], v12
	ds_read_b128 v[4:7], v12 offset:1024
	ds_read_b128 v[8:11], v12 offset:2048
	ds_read_b128 v[12:15], v12 offset:3072
	ds_read_b128 v[16:19], v28
	ds_read_b128 v[20:23], v28 offset:1024
	ds_read_b128 v[24:27], v28 offset:2048
	ds_read_b128 v[28:31], v28 offset:3072
	ds_read_b128 v[32:35], v209 offset:32768
	ds_read_b128 v[36:39], v209 offset:33792
	ds_read_b128 v[40:43], v209 offset:34816
	ds_read_b128 v[44:47], v209 offset:35840
	ds_read_b128 v[48:51], v209 offset:36864
	ds_read_b128 v[52:55], v209 offset:37888
	ds_read_b128 v[56:59], v209 offset:38912
	ds_read_b128 v[60:63], v209 offset:39936
	s_mov_b32 m0, s66
	s_nop 0
	global_load_lds_dwordx4 v66, s[40:41]
	s_mov_b32 m0, s67
	s_nop 0
	global_load_lds_dwordx4 v67, s[40:41]
	s_waitcnt vmcnt(8)
	s_waitcnt lgkmcnt(0)
	s_barrier
	s_setprio 1
	s_waitcnt lgkmcnt(6)
	v_mfma_scale_f32_16x16x128_f8f6f4 v[192:195], v[0:7], v[32:39], v[192:195], v210, v211 op_sel_hi:[0,0,0]
	v_mfma_scale_f32_16x16x128_f8f6f4 v[184:187], v[8:15], v[32:39], v[184:187], v210, v211 op_sel_hi:[0,0,0]
	s_waitcnt lgkmcnt(4)
	v_mfma_scale_f32_16x16x128_f8f6f4 v[176:179], v[0:7], v[40:47], v[176:179], v210, v211 op_sel_hi:[0,0,0]
	v_mfma_scale_f32_16x16x128_f8f6f4 v[168:171], v[8:15], v[40:47], v[168:171], v210, v211 op_sel_hi:[0,0,0]
	s_waitcnt lgkmcnt(2)
	v_mfma_scale_f32_16x16x128_f8f6f4 v[160:163], v[0:7], v[48:55], v[160:163], v210, v211 op_sel_hi:[0,0,0]
	v_mfma_scale_f32_16x16x128_f8f6f4 v[152:155], v[8:15], v[48:55], v[152:155], v210, v211 op_sel_hi:[0,0,0]
	s_waitcnt lgkmcnt(0)
	v_mfma_scale_f32_16x16x128_f8f6f4 v[144:147], v[0:7], v[56:63], v[144:147], v210, v211 op_sel_hi:[0,0,0]
	v_mfma_scale_f32_16x16x128_f8f6f4 v[136:139], v[8:15], v[56:63], v[136:139], v210, v211 op_sel_hi:[0,0,0]
	s_setprio 0
	s_setprio 1
	v_mfma_scale_f32_16x16x128_f8f6f4 v[188:191], v[16:23], v[32:39], v[188:191], v210, v211 op_sel_hi:[0,0,0]
	v_mfma_scale_f32_16x16x128_f8f6f4 v[180:183], v[24:31], v[32:39], v[180:183], v210, v211 op_sel_hi:[0,0,0]
	v_mfma_scale_f32_16x16x128_f8f6f4 v[172:175], v[16:23], v[40:47], v[172:175], v210, v211 op_sel_hi:[0,0,0]
	v_mfma_scale_f32_16x16x128_f8f6f4 v[164:167], v[24:31], v[40:47], v[164:167], v210, v211 op_sel_hi:[0,0,0]
	v_mfma_scale_f32_16x16x128_f8f6f4 v[156:159], v[16:23], v[48:55], v[156:159], v210, v211 op_sel_hi:[0,0,0]
	v_mfma_scale_f32_16x16x128_f8f6f4 v[148:151], v[24:31], v[48:55], v[148:151], v210, v211 op_sel_hi:[0,0,0]
	v_mfma_scale_f32_16x16x128_f8f6f4 v[140:143], v[16:23], v[56:63], v[140:143], v210, v211 op_sel_hi:[0,0,0]
	v_mfma_scale_f32_16x16x128_f8f6f4 v[132:135], v[24:31], v[56:63], v[132:135], v210, v211 op_sel_hi:[0,0,0]
	s_setprio 0
	s_barrier
	ds_read_b128 v[32:35], v209 offset:49152
	ds_read_b128 v[36:39], v209 offset:50176
	ds_read_b128 v[40:43], v209 offset:51200
	ds_read_b128 v[44:47], v209 offset:52224
	ds_read_b128 v[48:51], v209 offset:53248
	ds_read_b128 v[52:55], v209 offset:54272
	ds_read_b128 v[56:59], v209 offset:55296
	ds_read_b128 v[60:63], v209 offset:56320
	s_mov_b32 m0, s69
	s_nop 0
	global_load_lds_dwordx4 v200, s[38:39]
	s_mov_b32 m0, s70
	s_nop 0
	global_load_lds_dwordx4 v202, s[38:39]
	s_add_u32 s38, s38, s16
	s_addc_u32 s39, s39, s17
	s_mov_b32 m0, s73
	s_nop 0
	global_load_lds_dwordx4 v200, s[38:39]
	s_mov_b32 m0, s74
	s_nop 0
	global_load_lds_dwordx4 v202, s[38:39]
	s_mov_b32 m0, s71
	s_nop 0
	global_load_lds_dwordx4 v64, s[8:9]
	s_mov_b32 m0, s72
	s_nop 0
	global_load_lds_dwordx4 v65, s[8:9]
	s_waitcnt vmcnt(8)
	s_waitcnt lgkmcnt(0)
	s_barrier
	s_setprio 1
	s_waitcnt lgkmcnt(6)
	v_mfma_scale_f32_16x16x128_f8f6f4 v[128:131], v[0:7], v[32:39], v[128:131], v210, v211 op_sel_hi:[0,0,0]
	v_mfma_scale_f32_16x16x128_f8f6f4 v[120:123], v[8:15], v[32:39], v[120:123], v210, v211 op_sel_hi:[0,0,0]
	s_waitcnt lgkmcnt(4)
	v_mfma_scale_f32_16x16x128_f8f6f4 v[112:115], v[0:7], v[40:47], v[112:115], v210, v211 op_sel_hi:[0,0,0]
	v_mfma_scale_f32_16x16x128_f8f6f4 v[104:107], v[8:15], v[40:47], v[104:107], v210, v211 op_sel_hi:[0,0,0]
	s_waitcnt lgkmcnt(2)
	v_mfma_scale_f32_16x16x128_f8f6f4 v[96:99], v[0:7], v[48:55], v[96:99], v210, v211 op_sel_hi:[0,0,0]
	v_mfma_scale_f32_16x16x128_f8f6f4 v[88:91], v[8:15], v[48:55], v[88:91], v210, v211 op_sel_hi:[0,0,0]
	s_waitcnt lgkmcnt(0)
	v_mfma_scale_f32_16x16x128_f8f6f4 v[80:83], v[0:7], v[56:63], v[80:83], v210, v211 op_sel_hi:[0,0,0]
	v_mfma_scale_f32_16x16x128_f8f6f4 v[72:75], v[8:15], v[56:63], v[72:75], v210, v211 op_sel_hi:[0,0,0]
	s_setprio 0
	s_setprio 1
	v_mfma_scale_f32_16x16x128_f8f6f4 v[124:127], v[16:23], v[32:39], v[124:127], v210, v211 op_sel_hi:[0,0,0]
	v_mfma_scale_f32_16x16x128_f8f6f4 v[116:119], v[24:31], v[32:39], v[116:119], v210, v211 op_sel_hi:[0,0,0]
	v_mfma_scale_f32_16x16x128_f8f6f4 v[108:111], v[16:23], v[40:47], v[108:111], v210, v211 op_sel_hi:[0,0,0]
	v_mfma_scale_f32_16x16x128_f8f6f4 v[100:103], v[24:31], v[40:47], v[100:103], v210, v211 op_sel_hi:[0,0,0]
	v_mfma_scale_f32_16x16x128_f8f6f4 v[92:95], v[16:23], v[48:55], v[92:95], v210, v211 op_sel_hi:[0,0,0]
	v_mfma_scale_f32_16x16x128_f8f6f4 v[84:87], v[24:31], v[48:55], v[84:87], v210, v211 op_sel_hi:[0,0,0]
	v_mfma_scale_f32_16x16x128_f8f6f4 v[76:79], v[16:23], v[56:63], v[76:79], v210, v211 op_sel_hi:[0,0,0]
	v_mfma_scale_f32_16x16x128_f8f6f4 v[68:71], v[24:31], v[56:63], v[68:71], v210, v211 op_sel_hi:[0,0,0]
	s_add_u32 s6, s6, 0x100
	s_addc_u32 s7, s7, 0
	s_cmp_ge_i32 s82, s68
	s_setprio 0
	s_barrier
	s_cbranch_scc1 .LBB0_749

; #define PG8_STAGE(bufoff, gbase, voff) do { _Pragma("unroll") for (int _i = 0; _i < 2; ++_i) { unsigned keep_; \
;         asm volatile("s_mov_b32 %0, m0\n\ts_mov_b32 m0, %3\n\ts_nop 0\n\tglobal_load_lds_dwordx4 %1, %2\n\ts_mov_b32 m0, %0" : "=&s"(keep_) : "v"((voff)[_i]), "s"((const char*)(gbase)), "s"(ldsb + (unsigned)((bufoff) + _i * 8192)) : "memory"); } } while (0)
; #define PG8_LDA(dst, b, h) do { _Pragma("unroll") for (int m = 0; m < 4; ++m) _Pragma("unroll") for (int k = 0; k < 2; ++k) dst[m][k] = *(const PG8_LAS bf16x8*)(lds + PG8_SA(b, h) + aoff + m * 2048 + k * 1024); } while (0)
; #define PG8_LDB(dst, b, h) do { _Pragma("unroll") for (int n = 0; n < 2; ++n) _Pragma("unroll") for (int k = 0; k < 2; ++k) dst[n][k] = *(const PG8_LAS bf16x8*)(lds + PG8_SB(b, h) + boff + n * 2048 + k * 1024); } while (0)
; #define PG8_WAIT_V(n) asm volatile("s_waitcnt vmcnt(" #n ")" ::: "memory")
; #define PG8_WAIT_L(n) asm volatile("s_waitcnt lgkmcnt(" #n ")" ::: "memory")
; #define PG8_BAR __builtin_amdgcn_s_barrier()
; #define PG8_SCHED __builtin_amdgcn_sched_barrier(0)
; template <class Epi, class Sched, bool ALIGN_EPI, bool FP8 = false>
; __device__ __forceinline__ void gemm_phase(PG8_LAS unsigned char* lds, const Gemm g, const Sched& S, const Epi& E, const int wid, const int lane) {
;     ...
;         for (int t = 0; t < nt; t += 2) {
;             const bool last = (t == nt - 2);
;             const char* a1 = cA + (size_t)(t + 1) * kstep;
;             const char* a2 = last ? nA : cA + (size_t)(t + 2) * kstep; const char* b2 = last ? nB : cB + (size_t)(t + 2) * kstep;
;             const char* a3 = a2 + kstep; const char* b3 = b2 + kstep;
;             PG8_LDB(B0, 0, 0); PG8_LDB(B1, 0, 1); PG8_SCHED; PG8_LDA(At, 0, 0); PG8_STAGE(PG8_SA(1, 1), a1 + hstepA, vc1);
;             if (GA && last && has_next) { const u32x4 q = *gslot; vc0[0] = q.x; vc0[1] = q.y; vc1[0] = q.z; vc1[1] = q.w; }
;             PG8_WAIT_V(8); PG8_WAIT_L(0); PG8_BAR; PG8_MMA(0, 0, At, B0); PG8_MMA(0, 1, At, B1); PG8_BAR; PG8_SCHED;
;             PG8_LDA(At, 0, 1); PG8_STAGE(PG8_SB(0, 0), b2, voffB); PG8_STAGE(PG8_SB(0, 1), b2 + hstep, voffB); PG8_STAGE(PG8_SA(0, 0), a2, vc0);
;             PG8_WAIT_V(8); PG8_WAIT_L(0); PG8_BAR; PG8_MMA(1, 0, At, B0); PG8_MMA(1, 1, At, B1); PG8_BAR; PG8_SCHED;
.LBB0_852:
	ds_read_b128 v[24:27], v165
	ds_read_b128 v[28:31], v165 offset:1024
	ds_read_b128 v[16:19], v165 offset:2048
	ds_read_b128 v[20:23], v165 offset:3072
	ds_read_b128 v[8:11], v167
	ds_read_b128 v[12:15], v167 offset:1024
	ds_read_b128 v[0:3], v167 offset:2048
	ds_read_b128 v[4:7], v167 offset:3072
	s_add_i32 s33, s8, 2
	s_cmp_eq_u32 s67, s8
	s_cselect_b32 s36, s28, s75
	s_cselect_b32 s37, s29, s82
	s_cselect_b32 s34, s30, s83
	s_cselect_b32 s35, s31, s84
	s_add_u32 s8, s36, 0x80
	s_addc_u32 s9, s37, 0
	ds_read_b128 v[174:177], v169
	ds_read_b128 v[178:181], v169 offset:1024
	ds_read_b128 v[182:185], v169 offset:2048
	ds_read_b128 v[186:189], v169 offset:3072
	ds_read_b128 v[190:193], v169 offset:4096
	ds_read_b128 v[194:197], v169 offset:5120
	ds_read_b128 v[198:201], v169 offset:6144
	ds_read_b128 v[202:205], v169 offset:7168
	s_mov_b32 m0, s68
	s_nop 0
	global_load_lds_dwordx4 v160, s[6:7]
	s_mov_b32 m0, s69
	s_nop 0
	global_load_lds_dwordx4 v164, s[6:7]
	s_waitcnt vmcnt(8)
	s_waitcnt lgkmcnt(0)
	s_barrier
	s_setprio 1
	s_waitcnt lgkmcnt(6)
	v_mfma_scale_f32_16x16x128_f8f6f4 v[156:159], v[24:31], v[174:181], v[156:159], v170, v171 op_sel_hi:[0,0,0]
	v_mfma_scale_f32_16x16x128_f8f6f4 v[152:155], v[16:23], v[174:181], v[152:155], v170, v171 op_sel_hi:[0,0,0]
	s_waitcnt lgkmcnt(4)
	v_mfma_scale_f32_16x16x128_f8f6f4 v[140:143], v[24:31], v[182:189], v[140:143], v170, v171 op_sel_hi:[0,0,0]
	v_mfma_scale_f32_16x16x128_f8f6f4 v[136:139], v[16:23], v[182:189], v[136:139], v170, v171 op_sel_hi:[0,0,0]
	s_waitcnt lgkmcnt(2)
	v_mfma_scale_f32_16x16x128_f8f6f4 v[124:127], v[24:31], v[190:197], v[124:127], v170, v171 op_sel_hi:[0,0,0]
	v_mfma_scale_f32_16x16x128_f8f6f4 v[120:123], v[16:23], v[190:197], v[120:123], v170, v171 op_sel_hi:[0,0,0]
	s_waitcnt lgkmcnt(0)
	v_mfma_scale_f32_16x16x128_f8f6f4 v[108:111], v[24:31], v[198:205], v[108:111], v170, v171 op_sel_hi:[0,0,0]
	v_mfma_scale_f32_16x16x128_f8f6f4 v[104:107], v[16:23], v[198:205], v[104:107], v170, v171 op_sel_hi:[0,0,0]
	s_setprio 0
	s_setprio 1
	v_mfma_scale_f32_16x16x128_f8f6f4 v[148:151], v[8:15], v[174:181], v[148:151], v170, v171 op_sel_hi:[0,0,0]
	v_mfma_scale_f32_16x16x128_f8f6f4 v[144:147], v[0:7], v[174:181], v[144:147], v170, v171 op_sel_hi:[0,0,0]
	v_mfma_scale_f32_16x16x128_f8f6f4 v[132:135], v[8:15], v[182:189], v[132:135], v170, v171 op_sel_hi:[0,0,0]
	v_mfma_scale_f32_16x16x128_f8f6f4 v[128:131], v[0:7], v[182:189], v[128:131], v170, v171 op_sel_hi:[0,0,0]
	v_mfma_scale_f32_16x16x128_f8f6f4 v[116:119], v[8:15], v[190:197], v[116:119], v170, v171 op_sel_hi:[0,0,0]
	v_mfma_scale_f32_16x16x128_f8f6f4 v[112:115], v[0:7], v[190:197], v[112:115], v170, v171 op_sel_hi:[0,0,0]
	v_mfma_scale_f32_16x16x128_f8f6f4 v[100:103], v[8:15], v[198:205], v[100:103], v170, v171 op_sel_hi:[0,0,0]
	v_mfma_scale_f32_16x16x128_f8f6f4 v[96:99], v[0:7], v[198:205], v[96:99], v170, v171 op_sel_hi:[0,0,0]
	s_setprio 0
	s_barrier
	ds_read_b128 v[174:177], v169 offset:16384
	ds_read_b128 v[178:181], v169 offset:17408
	ds_read_b128 v[182:185], v169 offset:18432
	ds_read_b128 v[186:189], v169 offset:19456
	ds_read_b128 v[190:193], v169 offset:20480
	ds_read_b128 v[194:197], v169 offset:21504
	ds_read_b128 v[198:201], v169 offset:22528
	ds_read_b128 v[202:205], v169 offset:23552
	s_mov_b32 m0, s45
	s_nop 0
	global_load_lds_dwordx4 v162, s[34:35]
	s_mov_b32 m0, s46
	s_nop 0
	global_load_lds_dwordx4 v166, s[34:35]
	s_add_u32 s58, s34, s12
	s_addc_u32 s59, s35, s13
	s_mov_b32 m0, s47
	s_nop 0
	global_load_lds_dwordx4 v162, s[58:59]
	s_mov_b32 m0, s48
	s_nop 0
	global_load_lds_dwordx4 v166, s[58:59]
	s_mov_b32 m0, s40
	s_nop 0
	global_load_lds_dwordx4 v160, s[36:37]
	s_mov_b32 m0, s49
	s_nop 0
	global_load_lds_dwordx4 v164, s[36:37]
	s_waitcnt vmcnt(8)
	s_waitcnt lgkmcnt(0)
	s_barrier
	s_setprio 1
	s_waitcnt lgkmcnt(6)
	v_mfma_scale_f32_16x16x128_f8f6f4 v[92:95], v[24:31], v[174:181], v[92:95], v170, v171 op_sel_hi:[0,0,0]
	v_mfma_scale_f32_16x16x128_f8f6f4 v[88:91], v[16:23], v[174:181], v[88:91], v170, v171 op_sel_hi:[0,0,0]
	s_waitcnt lgkmcnt(4)
	v_mfma_scale_f32_16x16x128_f8f6f4 v[76:79], v[24:31], v[182:189], v[76:79], v170, v171 op_sel_hi:[0,0,0]
	v_mfma_scale_f32_16x16x128_f8f6f4 v[72:75], v[16:23], v[182:189], v[72:75], v170, v171 op_sel_hi:[0,0,0]
	s_waitcnt lgkmcnt(2)
	v_mfma_scale_f32_16x16x128_f8f6f4 v[60:63], v[24:31], v[190:197], v[60:63], v170, v171 op_sel_hi:[0,0,0]
	v_mfma_scale_f32_16x16x128_f8f6f4 v[56:59], v[16:23], v[190:197], v[56:59], v170, v171 op_sel_hi:[0,0,0]
	s_waitcnt lgkmcnt(0)
	v_mfma_scale_f32_16x16x128_f8f6f4 v[44:47], v[24:31], v[198:205], v[44:47], v170, v171 op_sel_hi:[0,0,0]
	v_mfma_scale_f32_16x16x128_f8f6f4 v[40:43], v[16:23], v[198:205], v[40:43], v170, v171 op_sel_hi:[0,0,0]
	s_setprio 0
	s_setprio 1
	v_mfma_scale_f32_16x16x128_f8f6f4 v[84:87], v[8:15], v[174:181], v[84:87], v170, v171 op_sel_hi:[0,0,0]
	v_mfma_scale_f32_16x16x128_f8f6f4 v[80:83], v[0:7], v[174:181], v[80:83], v170, v171 op_sel_hi:[0,0,0]
	v_mfma_scale_f32_16x16x128_f8f6f4 v[68:71], v[8:15], v[182:189], v[68:71], v170, v171 op_sel_hi:[0,0,0]
	v_mfma_scale_f32_16x16x128_f8f6f4 v[64:67], v[0:7], v[182:189], v[64:67], v170, v171 op_sel_hi:[0,0,0]
	v_mfma_scale_f32_16x16x128_f8f6f4 v[52:55], v[8:15], v[190:197], v[52:55], v170, v171 op_sel_hi:[0,0,0]
	v_mfma_scale_f32_16x16x128_f8f6f4 v[48:51], v[0:7], v[190:197], v[48:51], v170, v171 op_sel_hi:[0,0,0]
	v_mfma_scale_f32_16x16x128_f8f6f4 v[36:39], v[8:15], v[198:205], v[36:39], v170, v171 op_sel_hi:[0,0,0]
	v_mfma_scale_f32_16x16x128_f8f6f4 v[32:35], v[0:7], v[198:205], v[32:35], v170, v171 op_sel_hi:[0,0,0]
	s_setprio 0
	s_barrier
; #define PG8_STAGE(bufoff, gbase, voff) do { _Pragma("unroll") for (int _i = 0; _i < 2; ++_i) { unsigned keep_; \
;         asm volatile("s_mov_b32 %0, m0\n\ts_mov_b32 m0, %3\n\ts_nop 0\n\tglobal_load_lds_dwordx4 %1, %2\n\ts_mov_b32 m0, %0" : "=&s"(keep_) : "v"((voff)[_i]), "s"((const char*)(gbase)), "s"(ldsb + (unsigned)((bufoff) + _i * 8192)) : "memory"); } } while (0)
; #define PG8_LDA(dst, b, h) do { _Pragma("unroll") for (int m = 0; m < 4; ++m) _Pragma("unroll") for (int k = 0; k < 2; ++k) dst[m][k] = *(const PG8_LAS bf16x8*)(lds + PG8_SA(b, h) + aoff + m * 2048 + k * 1024); } while (0)
; #define PG8_LDB(dst, b, h) do { _Pragma("unroll") for (int n = 0; n < 2; ++n) _Pragma("unroll") for (int k = 0; k < 2; ++k) dst[n][k] = *(const PG8_LAS bf16x8*)(lds + PG8_SB(b, h) + boff + n * 2048 + k * 1024); } while (0)
; #define PG8_WAIT_V(n) asm volatile("s_waitcnt vmcnt(" #n ")" ::: "memory")
; #define PG8_WAIT_L(n) asm volatile("s_waitcnt lgkmcnt(" #n ")" ::: "memory")
; #define PG8_BAR __builtin_amdgcn_s_barrier()
; #define PG8_SCHED __builtin_amdgcn_sched_barrier(0)
; template <class Epi, class Sched, bool ALIGN_EPI, bool FP8 = false>
; __device__ __forceinline__ void gemm_phase(PG8_LAS unsigned char* lds, const Gemm g, const Sched& S, const Epi& E, const int wid, const int lane) {
;     ...
;             PG8_LDB(B0, 1, 0); PG8_LDB(B1, 1, 1); PG8_SCHED; PG8_LDA(At, 1, 0); PG8_STAGE(PG8_SA(0, 1), a2 + hstepA, vc1);
;             PG8_WAIT_V(8); PG8_WAIT_L(0); PG8_BAR; PG8_MMA(0, 0, At, B0); PG8_MMA(0, 1, At, B1); PG8_BAR; PG8_SCHED;
;             PG8_LDA(At, 1, 1); PG8_STAGE(PG8_SB(1, 0), b3, voffB); PG8_STAGE(PG8_SB(1, 1), b3 + hstep, voffB); PG8_STAGE(PG8_SA(1, 0), a3, vc0);
;             PG8_WAIT_V(8); PG8_WAIT_L(0); PG8_BAR; PG8_MMA(1, 0, At, B0); PG8_MMA(1, 1, At, B1); PG8_BAR; PG8_SCHED;
;         }
	ds_read_b128 v[0:3], v172
	ds_read_b128 v[4:7], v172 offset:1024
	ds_read_b128 v[8:11], v172 offset:2048
	ds_read_b128 v[12:15], v172 offset:3072
	ds_read_b128 v[16:19], v173
	ds_read_b128 v[20:23], v173 offset:1024
	ds_read_b128 v[24:27], v173 offset:2048
	ds_read_b128 v[28:31], v173 offset:3072
	ds_read_b128 v[174:177], v169 offset:32768
	ds_read_b128 v[178:181], v169 offset:33792
	ds_read_b128 v[182:185], v169 offset:34816
	ds_read_b128 v[186:189], v169 offset:35840
	ds_read_b128 v[190:193], v169 offset:36864
	ds_read_b128 v[194:197], v169 offset:37888
	ds_read_b128 v[198:201], v169 offset:38912
	ds_read_b128 v[202:205], v169 offset:39936
	s_add_u32 s36, s36, s12
	s_addc_u32 s37, s37, s13
	s_mov_b32 m0, s50
	s_nop 0
	global_load_lds_dwordx4 v160, s[36:37]
	s_mov_b32 m0, s51
	s_nop 0
	global_load_lds_dwordx4 v164, s[36:37]
	s_waitcnt vmcnt(8)
	s_waitcnt lgkmcnt(0)
	s_barrier
	s_setprio 1
	s_waitcnt lgkmcnt(6)
	v_mfma_scale_f32_16x16x128_f8f6f4 v[156:159], v[0:7], v[174:181], v[156:159], v170, v171 op_sel_hi:[0,0,0]
	v_mfma_scale_f32_16x16x128_f8f6f4 v[152:155], v[8:15], v[174:181], v[152:155], v170, v171 op_sel_hi:[0,0,0]
	s_waitcnt lgkmcnt(4)
	v_mfma_scale_f32_16x16x128_f8f6f4 v[140:143], v[0:7], v[182:189], v[140:143], v170, v171 op_sel_hi:[0,0,0]
	v_mfma_scale_f32_16x16x128_f8f6f4 v[136:139], v[8:15], v[182:189], v[136:139], v170, v171 op_sel_hi:[0,0,0]
	s_waitcnt lgkmcnt(2)
	v_mfma_scale_f32_16x16x128_f8f6f4 v[124:127], v[0:7], v[190:197], v[124:127], v170, v171 op_sel_hi:[0,0,0]
	v_mfma_scale_f32_16x16x128_f8f6f4 v[120:123], v[8:15], v[190:197], v[120:123], v170, v171 op_sel_hi:[0,0,0]
	s_waitcnt lgkmcnt(0)
	v_mfma_scale_f32_16x16x128_f8f6f4 v[108:111], v[0:7], v[198:205], v[108:111], v170, v171 op_sel_hi:[0,0,0]
	v_mfma_scale_f32_16x16x128_f8f6f4 v[104:107], v[8:15], v[198:205], v[104:107], v170, v171 op_sel_hi:[0,0,0]
	s_setprio 0
	s_setprio 1
	v_mfma_scale_f32_16x16x128_f8f6f4 v[148:151], v[16:23], v[174:181], v[148:151], v170, v171 op_sel_hi:[0,0,0]
	v_mfma_scale_f32_16x16x128_f8f6f4 v[144:147], v[24:31], v[174:181], v[144:147], v170, v171 op_sel_hi:[0,0,0]
	v_mfma_scale_f32_16x16x128_f8f6f4 v[132:135], v[16:23], v[182:189], v[132:135], v170, v171 op_sel_hi:[0,0,0]
	v_mfma_scale_f32_16x16x128_f8f6f4 v[128:131], v[24:31], v[182:189], v[128:131], v170, v171 op_sel_hi:[0,0,0]
	v_mfma_scale_f32_16x16x128_f8f6f4 v[116:119], v[16:23], v[190:197], v[116:119], v170, v171 op_sel_hi:[0,0,0]
	v_mfma_scale_f32_16x16x128_f8f6f4 v[112:115], v[24:31], v[190:197], v[112:115], v170, v171 op_sel_hi:[0,0,0]
	v_mfma_scale_f32_16x16x128_f8f6f4 v[100:103], v[16:23], v[198:205], v[100:103], v170, v171 op_sel_hi:[0,0,0]
	v_mfma_scale_f32_16x16x128_f8f6f4 v[96:99], v[24:31], v[198:205], v[96:99], v170, v171 op_sel_hi:[0,0,0]
	s_setprio 0
	s_barrier
	ds_read_b128 v[174:177], v169 offset:49152
	ds_read_b128 v[178:181], v169 offset:50176
	ds_read_b128 v[182:185], v169 offset:51200
	ds_read_b128 v[186:189], v169 offset:52224
	ds_read_b128 v[190:193], v169 offset:53248
	ds_read_b128 v[194:197], v169 offset:54272
	ds_read_b128 v[198:201], v169 offset:55296
	ds_read_b128 v[202:205], v169 offset:56320
	s_add_u32 s34, s34, 0x80
	s_addc_u32 s35, s35, 0
	s_mov_b32 m0, s53
	s_nop 0
	global_load_lds_dwordx4 v162, s[34:35]
	s_mov_b32 m0, s54
	s_nop 0
	global_load_lds_dwordx4 v166, s[34:35]
	s_add_u32 s34, s34, s12
	s_addc_u32 s35, s35, s13
	s_mov_b32 m0, s65
	s_nop 0
	global_load_lds_dwordx4 v162, s[34:35]
	s_mov_b32 m0, s66
	s_nop 0
	global_load_lds_dwordx4 v166, s[34:35]
	s_mov_b32 m0, s55
	s_nop 0
	global_load_lds_dwordx4 v160, s[8:9]
	s_mov_b32 m0, s64
	s_nop 0
	global_load_lds_dwordx4 v164, s[8:9]
	s_waitcnt vmcnt(8)
	s_waitcnt lgkmcnt(0)
	s_barrier
	s_setprio 1
	s_waitcnt lgkmcnt(6)
	v_mfma_scale_f32_16x16x128_f8f6f4 v[92:95], v[0:7], v[174:181], v[92:95], v170, v171 op_sel_hi:[0,0,0]
	v_mfma_scale_f32_16x16x128_f8f6f4 v[88:91], v[8:15], v[174:181], v[88:91], v170, v171 op_sel_hi:[0,0,0]
	s_waitcnt lgkmcnt(4)
	v_mfma_scale_f32_16x16x128_f8f6f4 v[76:79], v[0:7], v[182:189], v[76:79], v170, v171 op_sel_hi:[0,0,0]
	v_mfma_scale_f32_16x16x128_f8f6f4 v[72:75], v[8:15], v[182:189], v[72:75], v170, v171 op_sel_hi:[0,0,0]
	s_waitcnt lgkmcnt(2)
	v_mfma_scale_f32_16x16x128_f8f6f4 v[60:63], v[0:7], v[190:197], v[60:63], v170, v171 op_sel_hi:[0,0,0]
	v_mfma_scale_f32_16x16x128_f8f6f4 v[56:59], v[8:15], v[190:197], v[56:59], v170, v171 op_sel_hi:[0,0,0]
	s_waitcnt lgkmcnt(0)
	v_mfma_scale_f32_16x16x128_f8f6f4 v[44:47], v[0:7], v[198:205], v[44:47], v170, v171 op_sel_hi:[0,0,0]
	v_mfma_scale_f32_16x16x128_f8f6f4 v[40:43], v[8:15], v[198:205], v[40:43], v170, v171 op_sel_hi:[0,0,0]
	s_setprio 0
	s_setprio 1
	v_mfma_scale_f32_16x16x128_f8f6f4 v[84:87], v[16:23], v[174:181], v[84:87], v170, v171 op_sel_hi:[0,0,0]
	v_mfma_scale_f32_16x16x128_f8f6f4 v[80:83], v[24:31], v[174:181], v[80:83], v170, v171 op_sel_hi:[0,0,0]
	v_mfma_scale_f32_16x16x128_f8f6f4 v[68:71], v[16:23], v[182:189], v[68:71], v170, v171 op_sel_hi:[0,0,0]
	v_mfma_scale_f32_16x16x128_f8f6f4 v[64:67], v[24:31], v[182:189], v[64:67], v170, v171 op_sel_hi:[0,0,0]
	v_mfma_scale_f32_16x16x128_f8f6f4 v[52:55], v[16:23], v[190:197], v[52:55], v170, v171 op_sel_hi:[0,0,0]
	v_mfma_scale_f32_16x16x128_f8f6f4 v[48:51], v[24:31], v[190:197], v[48:51], v170, v171 op_sel_hi:[0,0,0]
	v_mfma_scale_f32_16x16x128_f8f6f4 v[36:39], v[16:23], v[198:205], v[36:39], v170, v171 op_sel_hi:[0,0,0]
	v_mfma_scale_f32_16x16x128_f8f6f4 v[32:35], v[24:31], v[198:205], v[32:35], v170, v171 op_sel_hi:[0,0,0]
	s_add_u32 s75, s75, 0x100
	s_addc_u32 s82, s82, 0
	s_add_u32 s83, s83, 0x100
	s_addc_u32 s84, s84, 0
	s_add_u32 s6, s6, 0x100
	s_addc_u32 s7, s7, 0
	s_cmp_ge_i32 s33, s52
	s_mov_b32 s8, s33
	s_setprio 0
	s_barrier
	s_cbranch_scc0 .LBB0_852

; #define PG8_STAGE(bufoff, gbase, voff) do { _Pragma("unroll") for (int _i = 0; _i < 2; ++_i) { unsigned keep_; \
;         asm volatile("s_mov_b32 %0, m0\n\ts_mov_b32 m0, %3\n\ts_nop 0\n\tglobal_load_lds_dwordx4 %1, %2\n\ts_mov_b32 m0, %0" : "=&s"(keep_) : "v"((voff)[_i]), "s"((const char*)(gbase)), "s"(ldsb + (unsigned)((bufoff) + _i * 8192)) : "memory"); } } while (0)
; #define PG8_LDA(dst, b, h) do { _Pragma("unroll") for (int m = 0; m < 4; ++m) _Pragma("unroll") for (int k = 0; k < 2; ++k) dst[m][k] = *(const PG8_LAS bf16x8*)(lds + PG8_SA(b, h) + aoff + m * 2048 + k * 1024); } while (0)
; #define PG8_LDB(dst, b, h) do { _Pragma("unroll") for (int n = 0; n < 2; ++n) _Pragma("unroll") for (int k = 0; k < 2; ++k) dst[n][k] = *(const PG8_LAS bf16x8*)(lds + PG8_SB(b, h) + boff + n * 2048 + k * 1024); } while (0)
; #define PG8_WAIT_V(n) asm volatile("s_waitcnt vmcnt(" #n ")" ::: "memory")
; #define PG8_WAIT_L(n) asm volatile("s_waitcnt lgkmcnt(" #n ")" ::: "memory")
; #define PG8_BAR __builtin_amdgcn_s_barrier()
; #define PG8_SCHED __builtin_amdgcn_sched_barrier(0)
; template <class Epi, class Sched, bool ALIGN_EPI, bool FP8 = false>
; __device__ __forceinline__ void gemm_phase(PG8_LAS unsigned char* lds, const Gemm g, const Sched& S, const Epi& E, const int wid, const int lane) {
;     ...
;         for (int t = 0; t < nt; t += 2) {
;             const bool last = (t == nt - 2);
;             const char* a1 = cA + (size_t)(t + 1) * kstep;
;             const char* a2 = last ? nA : cA + (size_t)(t + 2) * kstep; const char* b2 = last ? nB : cB + (size_t)(t + 2) * kstep;
;             const char* a3 = a2 + kstep; const char* b3 = b2 + kstep;
;             PG8_LDB(B0, 0, 0); PG8_LDB(B1, 0, 1); PG8_SCHED; PG8_LDA(At, 0, 0); PG8_STAGE(PG8_SA(1, 1), a1 + hstepA, vc1);
;             if (GA && last && has_next) { const u32x4 q = *gslot; vc0[0] = q.x; vc0[1] = q.y; vc1[0] = q.z; vc1[1] = q.w; }
;             PG8_WAIT_V(8); PG8_WAIT_L(0); PG8_BAR; PG8_MMA(0, 0, At, B0); PG8_MMA(0, 1, At, B1); PG8_BAR; PG8_SCHED;
;             PG8_LDA(At, 0, 1); PG8_STAGE(PG8_SB(0, 0), b2, voffB); PG8_STAGE(PG8_SB(0, 1), b2 + hstep, voffB); PG8_STAGE(PG8_SA(0, 0), a2, vc0);
;             PG8_WAIT_V(8); PG8_WAIT_L(0); PG8_BAR; PG8_MMA(1, 0, At, B0); PG8_MMA(1, 1, At, B1); PG8_BAR; PG8_SCHED;
.LBB0_1454:
	ds_read_b128 v[24:27], v165
	ds_read_b128 v[28:31], v165 offset:1024
	ds_read_b128 v[16:19], v165 offset:2048
	ds_read_b128 v[20:23], v165 offset:3072
	ds_read_b128 v[8:11], v167
	ds_read_b128 v[12:15], v167 offset:1024
	ds_read_b128 v[0:3], v167 offset:2048
	ds_read_b128 v[4:7], v167 offset:3072
	s_add_i32 s33, s30, 2
	s_cmp_eq_u32 s66, s30
	s_cselect_b32 s36, s4, s84
	s_cselect_b32 s37, s5, s85
	s_cselect_b32 s34, s26, s86
	s_cselect_b32 s35, s27, s87
	s_add_u32 s30, s36, 0x80
	s_addc_u32 s31, s37, 0
	ds_read_b128 v[178:181], v173
	ds_read_b128 v[182:185], v173 offset:1024
	ds_read_b128 v[186:189], v173 offset:2048
	ds_read_b128 v[190:193], v173 offset:3072
	ds_read_b128 v[194:197], v173 offset:4096
	ds_read_b128 v[198:201], v173 offset:5120
	ds_read_b128 v[202:205], v173 offset:6144
	ds_read_b128 v[206:209], v173 offset:7168
	s_mov_b32 m0, s67
	s_nop 0
	global_load_lds_dwordx4 v160, s[28:29]
	s_mov_b32 m0, s68
	s_nop 0
	global_load_lds_dwordx4 v164, s[28:29]
	s_waitcnt vmcnt(8)
	s_waitcnt lgkmcnt(0)
	s_barrier
	s_setprio 1
	s_waitcnt lgkmcnt(6)
	v_mfma_scale_f32_16x16x128_f8f6f4 v[156:159], v[24:31], v[178:185], v[156:159], v174, v175 op_sel_hi:[0,0,0]
	v_mfma_scale_f32_16x16x128_f8f6f4 v[152:155], v[16:23], v[178:185], v[152:155], v174, v175 op_sel_hi:[0,0,0]
	s_waitcnt lgkmcnt(4)
	v_mfma_scale_f32_16x16x128_f8f6f4 v[140:143], v[24:31], v[186:193], v[140:143], v174, v175 op_sel_hi:[0,0,0]
	v_mfma_scale_f32_16x16x128_f8f6f4 v[136:139], v[16:23], v[186:193], v[136:139], v174, v175 op_sel_hi:[0,0,0]
	s_waitcnt lgkmcnt(2)
	v_mfma_scale_f32_16x16x128_f8f6f4 v[124:127], v[24:31], v[194:201], v[124:127], v174, v175 op_sel_hi:[0,0,0]
	v_mfma_scale_f32_16x16x128_f8f6f4 v[120:123], v[16:23], v[194:201], v[120:123], v174, v175 op_sel_hi:[0,0,0]
	s_waitcnt lgkmcnt(0)
	v_mfma_scale_f32_16x16x128_f8f6f4 v[108:111], v[24:31], v[202:209], v[108:111], v174, v175 op_sel_hi:[0,0,0]
	v_mfma_scale_f32_16x16x128_f8f6f4 v[104:107], v[16:23], v[202:209], v[104:107], v174, v175 op_sel_hi:[0,0,0]
	s_setprio 0
	s_setprio 1
	v_mfma_scale_f32_16x16x128_f8f6f4 v[148:151], v[8:15], v[178:185], v[148:151], v174, v175 op_sel_hi:[0,0,0]
	v_mfma_scale_f32_16x16x128_f8f6f4 v[144:147], v[0:7], v[178:185], v[144:147], v174, v175 op_sel_hi:[0,0,0]
	v_mfma_scale_f32_16x16x128_f8f6f4 v[132:135], v[8:15], v[186:193], v[132:135], v174, v175 op_sel_hi:[0,0,0]
	v_mfma_scale_f32_16x16x128_f8f6f4 v[128:131], v[0:7], v[186:193], v[128:131], v174, v175 op_sel_hi:[0,0,0]
	v_mfma_scale_f32_16x16x128_f8f6f4 v[116:119], v[8:15], v[194:201], v[116:119], v174, v175 op_sel_hi:[0,0,0]
	v_mfma_scale_f32_16x16x128_f8f6f4 v[112:115], v[0:7], v[194:201], v[112:115], v174, v175 op_sel_hi:[0,0,0]
	v_mfma_scale_f32_16x16x128_f8f6f4 v[100:103], v[8:15], v[202:209], v[100:103], v174, v175 op_sel_hi:[0,0,0]
	v_mfma_scale_f32_16x16x128_f8f6f4 v[96:99], v[0:7], v[202:209], v[96:99], v174, v175 op_sel_hi:[0,0,0]
	s_setprio 0
	s_barrier
	ds_read_b128 v[178:181], v173 offset:16384
	ds_read_b128 v[182:185], v173 offset:17408
	ds_read_b128 v[186:189], v173 offset:18432
	ds_read_b128 v[190:193], v173 offset:19456
	ds_read_b128 v[194:197], v173 offset:20480
	ds_read_b128 v[198:201], v173 offset:21504
	ds_read_b128 v[202:205], v173 offset:22528
	ds_read_b128 v[206:209], v173 offset:23552
	s_mov_b32 m0, s44
	s_nop 0
	global_load_lds_dwordx4 v162, s[34:35]
	s_mov_b32 m0, s45
	s_nop 0
	global_load_lds_dwordx4 v166, s[34:35]
	s_add_u32 s58, s34, s6
	s_addc_u32 s59, s35, s7
	s_mov_b32 m0, s46
	s_nop 0
	global_load_lds_dwordx4 v162, s[58:59]
	s_mov_b32 m0, s47
	s_nop 0
	global_load_lds_dwordx4 v166, s[58:59]
	s_mov_b32 m0, s42
	s_nop 0
	global_load_lds_dwordx4 v160, s[36:37]
	s_mov_b32 m0, s48
	s_nop 0
	global_load_lds_dwordx4 v164, s[36:37]
	s_waitcnt vmcnt(8)
	s_waitcnt lgkmcnt(0)
	s_barrier
	s_setprio 1
	s_waitcnt lgkmcnt(6)
	v_mfma_scale_f32_16x16x128_f8f6f4 v[92:95], v[24:31], v[178:185], v[92:95], v174, v175 op_sel_hi:[0,0,0]
	v_mfma_scale_f32_16x16x128_f8f6f4 v[88:91], v[16:23], v[178:185], v[88:91], v174, v175 op_sel_hi:[0,0,0]
	s_waitcnt lgkmcnt(4)
	v_mfma_scale_f32_16x16x128_f8f6f4 v[76:79], v[24:31], v[186:193], v[76:79], v174, v175 op_sel_hi:[0,0,0]
	v_mfma_scale_f32_16x16x128_f8f6f4 v[72:75], v[16:23], v[186:193], v[72:75], v174, v175 op_sel_hi:[0,0,0]
	s_waitcnt lgkmcnt(2)
	v_mfma_scale_f32_16x16x128_f8f6f4 v[60:63], v[24:31], v[194:201], v[60:63], v174, v175 op_sel_hi:[0,0,0]
	v_mfma_scale_f32_16x16x128_f8f6f4 v[56:59], v[16:23], v[194:201], v[56:59], v174, v175 op_sel_hi:[0,0,0]
	s_waitcnt lgkmcnt(0)
	v_mfma_scale_f32_16x16x128_f8f6f4 v[44:47], v[24:31], v[202:209], v[44:47], v174, v175 op_sel_hi:[0,0,0]
	v_mfma_scale_f32_16x16x128_f8f6f4 v[40:43], v[16:23], v[202:209], v[40:43], v174, v175 op_sel_hi:[0,0,0]
	s_setprio 0
	s_setprio 1
	v_mfma_scale_f32_16x16x128_f8f6f4 v[84:87], v[8:15], v[178:185], v[84:87], v174, v175 op_sel_hi:[0,0,0]
	v_mfma_scale_f32_16x16x128_f8f6f4 v[80:83], v[0:7], v[178:185], v[80:83], v174, v175 op_sel_hi:[0,0,0]
	v_mfma_scale_f32_16x16x128_f8f6f4 v[68:71], v[8:15], v[186:193], v[68:71], v174, v175 op_sel_hi:[0,0,0]
	v_mfma_scale_f32_16x16x128_f8f6f4 v[64:67], v[0:7], v[186:193], v[64:67], v174, v175 op_sel_hi:[0,0,0]
	v_mfma_scale_f32_16x16x128_f8f6f4 v[52:55], v[8:15], v[194:201], v[52:55], v174, v175 op_sel_hi:[0,0,0]
	v_mfma_scale_f32_16x16x128_f8f6f4 v[48:51], v[0:7], v[194:201], v[48:51], v174, v175 op_sel_hi:[0,0,0]
	v_mfma_scale_f32_16x16x128_f8f6f4 v[36:39], v[8:15], v[202:209], v[36:39], v174, v175 op_sel_hi:[0,0,0]
	v_mfma_scale_f32_16x16x128_f8f6f4 v[32:35], v[0:7], v[202:209], v[32:35], v174, v175 op_sel_hi:[0,0,0]
	s_setprio 0
	s_barrier
; #define PG8_STAGE(bufoff, gbase, voff) do { _Pragma("unroll") for (int _i = 0; _i < 2; ++_i) { unsigned keep_; \
;         asm volatile("s_mov_b32 %0, m0\n\ts_mov_b32 m0, %3\n\ts_nop 0\n\tglobal_load_lds_dwordx4 %1, %2\n\ts_mov_b32 m0, %0" : "=&s"(keep_) : "v"((voff)[_i]), "s"((const char*)(gbase)), "s"(ldsb + (unsigned)((bufoff) + _i * 8192)) : "memory"); } } while (0)
; #define PG8_LDA(dst, b, h) do { _Pragma("unroll") for (int m = 0; m < 4; ++m) _Pragma("unroll") for (int k = 0; k < 2; ++k) dst[m][k] = *(const PG8_LAS bf16x8*)(lds + PG8_SA(b, h) + aoff + m * 2048 + k * 1024); } while (0)
; #define PG8_LDB(dst, b, h) do { _Pragma("unroll") for (int n = 0; n < 2; ++n) _Pragma("unroll") for (int k = 0; k < 2; ++k) dst[n][k] = *(const PG8_LAS bf16x8*)(lds + PG8_SB(b, h) + boff + n * 2048 + k * 1024); } while (0)
; #define PG8_WAIT_V(n) asm volatile("s_waitcnt vmcnt(" #n ")" ::: "memory")
; #define PG8_WAIT_L(n) asm volatile("s_waitcnt lgkmcnt(" #n ")" ::: "memory")
; #define PG8_BAR __builtin_amdgcn_s_barrier()
; #define PG8_SCHED __builtin_amdgcn_sched_barrier(0)
; template <class Epi, class Sched, bool ALIGN_EPI, bool FP8 = false>
; __device__ __forceinline__ void gemm_phase(PG8_LAS unsigned char* lds, const Gemm g, const Sched& S, const Epi& E, const int wid, const int lane) {
;     ...
;             PG8_LDB(B0, 1, 0); PG8_LDB(B1, 1, 1); PG8_SCHED; PG8_LDA(At, 1, 0); PG8_STAGE(PG8_SA(0, 1), a2 + hstepA, vc1);
;             PG8_WAIT_V(8); PG8_WAIT_L(0); PG8_BAR; PG8_MMA(0, 0, At, B0); PG8_MMA(0, 1, At, B1); PG8_BAR; PG8_SCHED;
;             PG8_LDA(At, 1, 1); PG8_STAGE(PG8_SB(1, 0), b3, voffB); PG8_STAGE(PG8_SB(1, 1), b3 + hstep, voffB); PG8_STAGE(PG8_SA(1, 0), a3, vc0);
;             PG8_WAIT_V(8); PG8_WAIT_L(0); PG8_BAR; PG8_MMA(1, 0, At, B0); PG8_MMA(1, 1, At, B1); PG8_BAR; PG8_SCHED;
;         }
	ds_read_b128 v[0:3], v176
	ds_read_b128 v[4:7], v176 offset:1024
	ds_read_b128 v[8:11], v176 offset:2048
	ds_read_b128 v[12:15], v176 offset:3072
	ds_read_b128 v[16:19], v177
	ds_read_b128 v[20:23], v177 offset:1024
	ds_read_b128 v[24:27], v177 offset:2048
	ds_read_b128 v[28:31], v177 offset:3072
	ds_read_b128 v[178:181], v173 offset:32768
	ds_read_b128 v[182:185], v173 offset:33792
	ds_read_b128 v[186:189], v173 offset:34816
	ds_read_b128 v[190:193], v173 offset:35840
	ds_read_b128 v[194:197], v173 offset:36864
	ds_read_b128 v[198:201], v173 offset:37888
	ds_read_b128 v[202:205], v173 offset:38912
	ds_read_b128 v[206:209], v173 offset:39936
	s_add_u32 s36, s36, s6
	s_addc_u32 s37, s37, s7
	s_mov_b32 m0, s49
	s_nop 0
	global_load_lds_dwordx4 v160, s[36:37]
	s_mov_b32 m0, s50
	s_nop 0
	global_load_lds_dwordx4 v164, s[36:37]
	s_waitcnt vmcnt(8)
	s_waitcnt lgkmcnt(0)
	s_barrier
	s_setprio 1
	s_waitcnt lgkmcnt(6)
	v_mfma_scale_f32_16x16x128_f8f6f4 v[156:159], v[0:7], v[178:185], v[156:159], v174, v175 op_sel_hi:[0,0,0]
	v_mfma_scale_f32_16x16x128_f8f6f4 v[152:155], v[8:15], v[178:185], v[152:155], v174, v175 op_sel_hi:[0,0,0]
	s_waitcnt lgkmcnt(4)
	v_mfma_scale_f32_16x16x128_f8f6f4 v[140:143], v[0:7], v[186:193], v[140:143], v174, v175 op_sel_hi:[0,0,0]
	v_mfma_scale_f32_16x16x128_f8f6f4 v[136:139], v[8:15], v[186:193], v[136:139], v174, v175 op_sel_hi:[0,0,0]
	s_waitcnt lgkmcnt(2)
	v_mfma_scale_f32_16x16x128_f8f6f4 v[124:127], v[0:7], v[194:201], v[124:127], v174, v175 op_sel_hi:[0,0,0]
	v_mfma_scale_f32_16x16x128_f8f6f4 v[120:123], v[8:15], v[194:201], v[120:123], v174, v175 op_sel_hi:[0,0,0]
	s_waitcnt lgkmcnt(0)
	v_mfma_scale_f32_16x16x128_f8f6f4 v[108:111], v[0:7], v[202:209], v[108:111], v174, v175 op_sel_hi:[0,0,0]
	v_mfma_scale_f32_16x16x128_f8f6f4 v[104:107], v[8:15], v[202:209], v[104:107], v174, v175 op_sel_hi:[0,0,0]
	s_setprio 0
	s_setprio 1
	v_mfma_scale_f32_16x16x128_f8f6f4 v[148:151], v[16:23], v[178:185], v[148:151], v174, v175 op_sel_hi:[0,0,0]
	v_mfma_scale_f32_16x16x128_f8f6f4 v[144:147], v[24:31], v[178:185], v[144:147], v174, v175 op_sel_hi:[0,0,0]
	v_mfma_scale_f32_16x16x128_f8f6f4 v[132:135], v[16:23], v[186:193], v[132:135], v174, v175 op_sel_hi:[0,0,0]
	v_mfma_scale_f32_16x16x128_f8f6f4 v[128:131], v[24:31], v[186:193], v[128:131], v174, v175 op_sel_hi:[0,0,0]
	v_mfma_scale_f32_16x16x128_f8f6f4 v[116:119], v[16:23], v[194:201], v[116:119], v174, v175 op_sel_hi:[0,0,0]
	v_mfma_scale_f32_16x16x128_f8f6f4 v[112:115], v[24:31], v[194:201], v[112:115], v174, v175 op_sel_hi:[0,0,0]
	v_mfma_scale_f32_16x16x128_f8f6f4 v[100:103], v[16:23], v[202:209], v[100:103], v174, v175 op_sel_hi:[0,0,0]
	v_mfma_scale_f32_16x16x128_f8f6f4 v[96:99], v[24:31], v[202:209], v[96:99], v174, v175 op_sel_hi:[0,0,0]
	s_setprio 0
	s_barrier
	ds_read_b128 v[178:181], v173 offset:49152
	ds_read_b128 v[182:185], v173 offset:50176
	ds_read_b128 v[186:189], v173 offset:51200
	ds_read_b128 v[190:193], v173 offset:52224
	ds_read_b128 v[194:197], v173 offset:53248
	ds_read_b128 v[198:201], v173 offset:54272
	ds_read_b128 v[202:205], v173 offset:55296
	ds_read_b128 v[206:209], v173 offset:56320
	s_add_u32 s34, s34, 0x80
	s_addc_u32 s35, s35, 0
	s_mov_b32 m0, s52
	s_nop 0
	global_load_lds_dwordx4 v162, s[34:35]
	s_mov_b32 m0, s53
	s_nop 0
	global_load_lds_dwordx4 v166, s[34:35]
	s_add_u32 s34, s34, s6
	s_addc_u32 s35, s35, s7
	s_mov_b32 m0, s64
	s_nop 0
	global_load_lds_dwordx4 v162, s[34:35]
	s_mov_b32 m0, s65
	s_nop 0
	global_load_lds_dwordx4 v166, s[34:35]
	s_mov_b32 m0, s54
	s_nop 0
	global_load_lds_dwordx4 v160, s[30:31]
	s_mov_b32 m0, s55
	s_nop 0
	global_load_lds_dwordx4 v164, s[30:31]
	s_waitcnt vmcnt(8)
	s_waitcnt lgkmcnt(0)
	s_barrier
	s_setprio 1
	s_waitcnt lgkmcnt(6)
	v_mfma_scale_f32_16x16x128_f8f6f4 v[92:95], v[0:7], v[178:185], v[92:95], v174, v175 op_sel_hi:[0,0,0]
	v_mfma_scale_f32_16x16x128_f8f6f4 v[88:91], v[8:15], v[178:185], v[88:91], v174, v175 op_sel_hi:[0,0,0]
	s_waitcnt lgkmcnt(4)
	v_mfma_scale_f32_16x16x128_f8f6f4 v[76:79], v[0:7], v[186:193], v[76:79], v174, v175 op_sel_hi:[0,0,0]
	v_mfma_scale_f32_16x16x128_f8f6f4 v[72:75], v[8:15], v[186:193], v[72:75], v174, v175 op_sel_hi:[0,0,0]
	s_waitcnt lgkmcnt(2)
	v_mfma_scale_f32_16x16x128_f8f6f4 v[60:63], v[0:7], v[194:201], v[60:63], v174, v175 op_sel_hi:[0,0,0]
	v_mfma_scale_f32_16x16x128_f8f6f4 v[56:59], v[8:15], v[194:201], v[56:59], v174, v175 op_sel_hi:[0,0,0]
	s_waitcnt lgkmcnt(0)
	v_mfma_scale_f32_16x16x128_f8f6f4 v[44:47], v[0:7], v[202:209], v[44:47], v174, v175 op_sel_hi:[0,0,0]
	v_mfma_scale_f32_16x16x128_f8f6f4 v[40:43], v[8:15], v[202:209], v[40:43], v174, v175 op_sel_hi:[0,0,0]
	s_setprio 0
	s_setprio 1
	v_mfma_scale_f32_16x16x128_f8f6f4 v[84:87], v[16:23], v[178:185], v[84:87], v174, v175 op_sel_hi:[0,0,0]
	v_mfma_scale_f32_16x16x128_f8f6f4 v[80:83], v[24:31], v[178:185], v[80:83], v174, v175 op_sel_hi:[0,0,0]
	v_mfma_scale_f32_16x16x128_f8f6f4 v[68:71], v[16:23], v[186:193], v[68:71], v174, v175 op_sel_hi:[0,0,0]
	v_mfma_scale_f32_16x16x128_f8f6f4 v[64:67], v[24:31], v[186:193], v[64:67], v174, v175 op_sel_hi:[0,0,0]
	v_mfma_scale_f32_16x16x128_f8f6f4 v[52:55], v[16:23], v[194:201], v[52:55], v174, v175 op_sel_hi:[0,0,0]
	v_mfma_scale_f32_16x16x128_f8f6f4 v[48:51], v[24:31], v[194:201], v[48:51], v174, v175 op_sel_hi:[0,0,0]
	v_mfma_scale_f32_16x16x128_f8f6f4 v[36:39], v[16:23], v[202:209], v[36:39], v174, v175 op_sel_hi:[0,0,0]
	v_mfma_scale_f32_16x16x128_f8f6f4 v[32:35], v[24:31], v[202:209], v[32:35], v174, v175 op_sel_hi:[0,0,0]
	s_add_u32 s84, s84, 0x100
	s_addc_u32 s85, s85, 0
	s_add_u32 s86, s86, 0x100
	s_addc_u32 s87, s87, 0
	s_add_u32 s28, s28, 0x100
	s_addc_u32 s29, s29, 0
	s_cmp_ge_i32 s33, s51
	s_mov_b32 s30, s33
	s_setprio 0
	s_barrier
	s_cbranch_scc0 .LBB0_1454

; #define PG8_STAGE(bufoff, gbase, voff) do { _Pragma("unroll") for (int _i = 0; _i < 2; ++_i) { unsigned keep_; \
;         asm volatile("s_mov_b32 %0, m0\n\ts_mov_b32 m0, %3\n\ts_nop 0\n\tglobal_load_lds_dwordx4 %1, %2\n\ts_mov_b32 m0, %0" : "=&s"(keep_) : "v"((voff)[_i]), "s"((const char*)(gbase)), "s"(ldsb + (unsigned)((bufoff) + _i * 8192)) : "memory"); } } while (0)
; #define PG8_LDA(dst, b, h) do { _Pragma("unroll") for (int m = 0; m < 4; ++m) _Pragma("unroll") for (int k = 0; k < 2; ++k) dst[m][k] = *(const PG8_LAS bf16x8*)(lds + PG8_SA(b, h) + aoff + m * 2048 + k * 1024); } while (0)
; #define PG8_LDB(dst, b, h) do { _Pragma("unroll") for (int n = 0; n < 2; ++n) _Pragma("unroll") for (int k = 0; k < 2; ++k) dst[n][k] = *(const PG8_LAS bf16x8*)(lds + PG8_SB(b, h) + boff + n * 2048 + k * 1024); } while (0)
; #define PG8_WAIT_V(n) asm volatile("s_waitcnt vmcnt(" #n ")" ::: "memory")
; #define PG8_WAIT_L(n) asm volatile("s_waitcnt lgkmcnt(" #n ")" ::: "memory")
; #define PG8_BAR __builtin_amdgcn_s_barrier()
; #define PG8_SCHED __builtin_amdgcn_sched_barrier(0)
; template <class Epi, class Sched, bool ALIGN_EPI, bool FP8 = false>
; __device__ __forceinline__ void gemm_phase(PG8_LAS unsigned char* lds, const Gemm g, const Sched& S, const Epi& E, const int wid, const int lane) {
;     ...
;         for (int t = 0; t < nt; t += 2) {
;             const bool last = (t == nt - 2);
;             const char* a1 = cA + (size_t)(t + 1) * kstep;
;             const char* a2 = last ? nA : cA + (size_t)(t + 2) * kstep; const char* b2 = last ? nB : cB + (size_t)(t + 2) * kstep;
;             const char* a3 = a2 + kstep; const char* b3 = b2 + kstep;
;             PG8_LDB(B0, 0, 0); PG8_LDB(B1, 0, 1); PG8_SCHED; PG8_LDA(At, 0, 0); PG8_STAGE(PG8_SA(1, 1), a1 + hstepA, vc1);
;             if (GA && last && has_next) { const u32x4 q = *gslot; vc0[0] = q.x; vc0[1] = q.y; vc1[0] = q.z; vc1[1] = q.w; }
;             PG8_WAIT_V(8); PG8_WAIT_L(0); PG8_BAR; PG8_MMA(0, 0, At, B0); PG8_MMA(0, 1, At, B1); PG8_BAR; PG8_SCHED;
;             PG8_LDA(At, 0, 1); PG8_STAGE(PG8_SB(0, 0), b2, voffB); PG8_STAGE(PG8_SB(0, 1), b2 + hstep, voffB); PG8_STAGE(PG8_SA(0, 0), a2, vc0);
;             PG8_WAIT_V(8); PG8_WAIT_L(0); PG8_BAR; PG8_MMA(1, 0, At, B0); PG8_MMA(1, 1, At, B1); PG8_BAR; PG8_SCHED;
.LBB0_1637:
	s_add_i32 s89, s89, 2
	s_and_b64 s[8:9], s[38:39], exec
	s_cselect_b32 s9, 0, s6
	s_cselect_b32 s8, 0, s7
	s_add_u32 s40, s20, s9
	s_addc_u32 s41, s21, s8
	s_add_u32 s33, s34, s6
	s_addc_u32 s42, s35, s7
	s_add_u32 s8, s40, 0x80
	s_addc_u32 s9, s41, 0
	s_waitcnt vmcnt(8)
	s_and_b64 s[38:39], s[38:39], exec
	s_waitcnt lgkmcnt(0)
	s_cselect_b32 s43, s31, s42
	s_cselect_b32 s42, s30, s33
	s_add_u32 s38, s42, 0x80
	s_addc_u32 s39, s43, 0
	s_barrier
	s_setprio 1
	s_waitcnt lgkmcnt(6)
	v_mfma_scale_f32_16x16x128_f8f6f4 v[192:195], v[24:31], v[56:63], v[192:195], v210, v211 op_sel_hi:[0,0,0]
	v_mfma_scale_f32_16x16x128_f8f6f4 v[184:187], v[16:23], v[56:63], v[184:187], v210, v211 op_sel_hi:[0,0,0]
	s_waitcnt lgkmcnt(4)
	v_mfma_scale_f32_16x16x128_f8f6f4 v[176:179], v[24:31], v[48:55], v[176:179], v210, v211 op_sel_hi:[0,0,0]
	v_mfma_scale_f32_16x16x128_f8f6f4 v[168:171], v[16:23], v[48:55], v[168:171], v210, v211 op_sel_hi:[0,0,0]
	s_waitcnt lgkmcnt(2)
	v_mfma_scale_f32_16x16x128_f8f6f4 v[160:163], v[24:31], v[40:47], v[160:163], v210, v211 op_sel_hi:[0,0,0]
	v_mfma_scale_f32_16x16x128_f8f6f4 v[152:155], v[16:23], v[40:47], v[152:155], v210, v211 op_sel_hi:[0,0,0]
	s_waitcnt lgkmcnt(0)
	v_mfma_scale_f32_16x16x128_f8f6f4 v[144:147], v[24:31], v[32:39], v[144:147], v210, v211 op_sel_hi:[0,0,0]
	v_mfma_scale_f32_16x16x128_f8f6f4 v[136:139], v[16:23], v[32:39], v[136:139], v210, v211 op_sel_hi:[0,0,0]
	s_setprio 0
	s_setprio 1
	v_mfma_scale_f32_16x16x128_f8f6f4 v[188:191], v[8:15], v[56:63], v[188:191], v210, v211 op_sel_hi:[0,0,0]
	v_mfma_scale_f32_16x16x128_f8f6f4 v[180:183], v[0:7], v[56:63], v[180:183], v210, v211 op_sel_hi:[0,0,0]
	v_mfma_scale_f32_16x16x128_f8f6f4 v[172:175], v[8:15], v[48:55], v[172:175], v210, v211 op_sel_hi:[0,0,0]
	v_mfma_scale_f32_16x16x128_f8f6f4 v[164:167], v[0:7], v[48:55], v[164:167], v210, v211 op_sel_hi:[0,0,0]
	v_mfma_scale_f32_16x16x128_f8f6f4 v[156:159], v[8:15], v[40:47], v[156:159], v210, v211 op_sel_hi:[0,0,0]
	v_mfma_scale_f32_16x16x128_f8f6f4 v[148:151], v[0:7], v[40:47], v[148:151], v210, v211 op_sel_hi:[0,0,0]
	v_mfma_scale_f32_16x16x128_f8f6f4 v[140:143], v[8:15], v[32:39], v[140:143], v210, v211 op_sel_hi:[0,0,0]
	v_mfma_scale_f32_16x16x128_f8f6f4 v[132:135], v[0:7], v[32:39], v[132:135], v210, v211 op_sel_hi:[0,0,0]
	s_setprio 0
	s_barrier
	ds_read_b128 v[32:35], v209 offset:16384
	ds_read_b128 v[36:39], v209 offset:17408
	ds_read_b128 v[40:43], v209 offset:18432
	ds_read_b128 v[44:47], v209 offset:19456
	ds_read_b128 v[48:51], v209 offset:20480
	ds_read_b128 v[52:55], v209 offset:21504
	ds_read_b128 v[56:59], v209 offset:22528
	ds_read_b128 v[60:63], v209 offset:23552
	s_mov_b32 m0, s51
	s_nop 0
	global_load_lds_dwordx4 v200, s[42:43]
	s_mov_b32 m0, s53
	s_nop 0
	global_load_lds_dwordx4 v202, s[42:43]
	s_add_u32 s42, s42, s16
	s_addc_u32 s43, s43, s17
	s_mov_b32 m0, s55
	s_nop 0
	global_load_lds_dwordx4 v200, s[42:43]
	s_mov_b32 m0, s64
	s_nop 0
	global_load_lds_dwordx4 v202, s[42:43]
	s_mov_b32 m0, s47
	s_nop 0
	global_load_lds_dwordx4 v64, s[40:41]
	s_mov_b32 m0, s65
	s_nop 0
	global_load_lds_dwordx4 v65, s[40:41]
	s_waitcnt vmcnt(8)
	s_waitcnt lgkmcnt(0)
	s_barrier
	s_setprio 1
	s_waitcnt lgkmcnt(6)
	v_mfma_scale_f32_16x16x128_f8f6f4 v[128:131], v[24:31], v[32:39], v[128:131], v210, v211 op_sel_hi:[0,0,0]
	v_mfma_scale_f32_16x16x128_f8f6f4 v[120:123], v[16:23], v[32:39], v[120:123], v210, v211 op_sel_hi:[0,0,0]
	s_waitcnt lgkmcnt(4)
	v_mfma_scale_f32_16x16x128_f8f6f4 v[112:115], v[24:31], v[40:47], v[112:115], v210, v211 op_sel_hi:[0,0,0]
	v_mfma_scale_f32_16x16x128_f8f6f4 v[104:107], v[16:23], v[40:47], v[104:107], v210, v211 op_sel_hi:[0,0,0]
	s_waitcnt lgkmcnt(2)
	v_mfma_scale_f32_16x16x128_f8f6f4 v[96:99], v[24:31], v[48:55], v[96:99], v210, v211 op_sel_hi:[0,0,0]
	v_mfma_scale_f32_16x16x128_f8f6f4 v[88:91], v[16:23], v[48:55], v[88:91], v210, v211 op_sel_hi:[0,0,0]
	s_waitcnt lgkmcnt(0)
	v_mfma_scale_f32_16x16x128_f8f6f4 v[80:83], v[24:31], v[56:63], v[80:83], v210, v211 op_sel_hi:[0,0,0]
	v_mfma_scale_f32_16x16x128_f8f6f4 v[72:75], v[16:23], v[56:63], v[72:75], v210, v211 op_sel_hi:[0,0,0]
	s_setprio 0
	s_setprio 1
	v_mfma_scale_f32_16x16x128_f8f6f4 v[124:127], v[8:15], v[32:39], v[124:127], v210, v211 op_sel_hi:[0,0,0]
	v_mfma_scale_f32_16x16x128_f8f6f4 v[116:119], v[0:7], v[32:39], v[116:119], v210, v211 op_sel_hi:[0,0,0]
	v_mfma_scale_f32_16x16x128_f8f6f4 v[108:111], v[8:15], v[40:47], v[108:111], v210, v211 op_sel_hi:[0,0,0]
	v_mfma_scale_f32_16x16x128_f8f6f4 v[100:103], v[0:7], v[40:47], v[100:103], v210, v211 op_sel_hi:[0,0,0]
	v_mfma_scale_f32_16x16x128_f8f6f4 v[92:95], v[8:15], v[48:55], v[92:95], v210, v211 op_sel_hi:[0,0,0]
	v_mfma_scale_f32_16x16x128_f8f6f4 v[84:87], v[0:7], v[48:55], v[84:87], v210, v211 op_sel_hi:[0,0,0]
	v_mfma_scale_f32_16x16x128_f8f6f4 v[76:79], v[8:15], v[56:63], v[76:79], v210, v211 op_sel_hi:[0,0,0]
	v_mfma_scale_f32_16x16x128_f8f6f4 v[68:71], v[0:7], v[56:63], v[68:71], v210, v211 op_sel_hi:[0,0,0]
	s_setprio 0
	s_barrier
; #define PG8_STAGE(bufoff, gbase, voff) do { _Pragma("unroll") for (int _i = 0; _i < 2; ++_i) { unsigned keep_; \
;         asm volatile("s_mov_b32 %0, m0\n\ts_mov_b32 m0, %3\n\ts_nop 0\n\tglobal_load_lds_dwordx4 %1, %2\n\ts_mov_b32 m0, %0" : "=&s"(keep_) : "v"((voff)[_i]), "s"((const char*)(gbase)), "s"(ldsb + (unsigned)((bufoff) + _i * 8192)) : "memory"); } } while (0)
; #define PG8_LDA(dst, b, h) do { _Pragma("unroll") for (int m = 0; m < 4; ++m) _Pragma("unroll") for (int k = 0; k < 2; ++k) dst[m][k] = *(const PG8_LAS bf16x8*)(lds + PG8_SA(b, h) + aoff + m * 2048 + k * 1024); } while (0)
; #define PG8_LDB(dst, b, h) do { _Pragma("unroll") for (int n = 0; n < 2; ++n) _Pragma("unroll") for (int k = 0; k < 2; ++k) dst[n][k] = *(const PG8_LAS bf16x8*)(lds + PG8_SB(b, h) + boff + n * 2048 + k * 1024); } while (0)
; #define PG8_WAIT_V(n) asm volatile("s_waitcnt vmcnt(" #n ")" ::: "memory")
; #define PG8_WAIT_L(n) asm volatile("s_waitcnt lgkmcnt(" #n ")" ::: "memory")
; #define PG8_BAR __builtin_amdgcn_s_barrier()
; #define PG8_SCHED __builtin_amdgcn_sched_barrier(0)
; template <class Epi, class Sched, bool ALIGN_EPI, bool FP8 = false>
; __device__ __forceinline__ void gemm_phase(PG8_LAS unsigned char* lds, const Gemm g, const Sched& S, const Epi& E, const int wid, const int lane) {
;     ...
;             PG8_LDB(B0, 1, 0); PG8_LDB(B1, 1, 1); PG8_SCHED; PG8_LDA(At, 1, 0); PG8_STAGE(PG8_SA(0, 1), a2 + hstepA, vc1);
;             PG8_WAIT_V(8); PG8_WAIT_L(0); PG8_BAR; PG8_MMA(0, 0, At, B0); PG8_MMA(0, 1, At, B1); PG8_BAR; PG8_SCHED;
;             PG8_LDA(At, 1, 1); PG8_STAGE(PG8_SB(1, 0), b3, voffB); PG8_STAGE(PG8_SB(1, 1), b3 + hstep, voffB); PG8_STAGE(PG8_SA(1, 0), a3, vc0);
;             PG8_WAIT_V(8); PG8_WAIT_L(0); PG8_BAR; PG8_MMA(1, 0, At, B0); PG8_MMA(1, 1, At, B1); PG8_BAR; PG8_SCHED;
;         }
	v_add_u32_e32 v12, 0x18000, v206
	v_add_u32_e32 v28, 0x1c000, v206
	ds_read_b128 v[0:3], v12
	ds_read_b128 v[4:7], v12 offset:1024
	ds_read_b128 v[8:11], v12 offset:2048
	ds_read_b128 v[12:15], v12 offset:3072
	ds_read_b128 v[16:19], v28
	ds_read_b128 v[20:23], v28 offset:1024
	ds_read_b128 v[24:27], v28 offset:2048
	ds_read_b128 v[28:31], v28 offset:3072
	ds_read_b128 v[32:35], v209 offset:32768
	ds_read_b128 v[36:39], v209 offset:33792
	ds_read_b128 v[40:43], v209 offset:34816
	ds_read_b128 v[44:47], v209 offset:35840
	ds_read_b128 v[48:51], v209 offset:36864
	ds_read_b128 v[52:55], v209 offset:37888
	ds_read_b128 v[56:59], v209 offset:38912
	ds_read_b128 v[60:63], v209 offset:39936
	s_mov_b32 m0, s66
	s_nop 0
	global_load_lds_dwordx4 v66, s[40:41]
	s_mov_b32 m0, s67
	s_nop 0
	global_load_lds_dwordx4 v67, s[40:41]
	s_waitcnt vmcnt(8)
	s_waitcnt lgkmcnt(0)
	s_barrier
	s_setprio 1
	s_waitcnt lgkmcnt(6)
	v_mfma_scale_f32_16x16x128_f8f6f4 v[192:195], v[0:7], v[32:39], v[192:195], v210, v211 op_sel_hi:[0,0,0]
	v_mfma_scale_f32_16x16x128_f8f6f4 v[184:187], v[8:15], v[32:39], v[184:187], v210, v211 op_sel_hi:[0,0,0]
	s_waitcnt lgkmcnt(4)
	v_mfma_scale_f32_16x16x128_f8f6f4 v[176:179], v[0:7], v[40:47], v[176:179], v210, v211 op_sel_hi:[0,0,0]
	v_mfma_scale_f32_16x16x128_f8f6f4 v[168:171], v[8:15], v[40:47], v[168:171], v210, v211 op_sel_hi:[0,0,0]
	s_waitcnt lgkmcnt(2)
	v_mfma_scale_f32_16x16x128_f8f6f4 v[160:163], v[0:7], v[48:55], v[160:163], v210, v211 op_sel_hi:[0,0,0]
	v_mfma_scale_f32_16x16x128_f8f6f4 v[152:155], v[8:15], v[48:55], v[152:155], v210, v211 op_sel_hi:[0,0,0]
	s_waitcnt lgkmcnt(0)
	v_mfma_scale_f32_16x16x128_f8f6f4 v[144:147], v[0:7], v[56:63], v[144:147], v210, v211 op_sel_hi:[0,0,0]
	v_mfma_scale_f32_16x16x128_f8f6f4 v[136:139], v[8:15], v[56:63], v[136:139], v210, v211 op_sel_hi:[0,0,0]
	s_setprio 0
	s_setprio 1
	v_mfma_scale_f32_16x16x128_f8f6f4 v[188:191], v[16:23], v[32:39], v[188:191], v210, v211 op_sel_hi:[0,0,0]
	v_mfma_scale_f32_16x16x128_f8f6f4 v[180:183], v[24:31], v[32:39], v[180:183], v210, v211 op_sel_hi:[0,0,0]
	v_mfma_scale_f32_16x16x128_f8f6f4 v[172:175], v[16:23], v[40:47], v[172:175], v210, v211 op_sel_hi:[0,0,0]
	v_mfma_scale_f32_16x16x128_f8f6f4 v[164:167], v[24:31], v[40:47], v[164:167], v210, v211 op_sel_hi:[0,0,0]
	v_mfma_scale_f32_16x16x128_f8f6f4 v[156:159], v[16:23], v[48:55], v[156:159], v210, v211 op_sel_hi:[0,0,0]
	v_mfma_scale_f32_16x16x128_f8f6f4 v[148:151], v[24:31], v[48:55], v[148:151], v210, v211 op_sel_hi:[0,0,0]
	v_mfma_scale_f32_16x16x128_f8f6f4 v[140:143], v[16:23], v[56:63], v[140:143], v210, v211 op_sel_hi:[0,0,0]
	v_mfma_scale_f32_16x16x128_f8f6f4 v[132:135], v[24:31], v[56:63], v[132:135], v210, v211 op_sel_hi:[0,0,0]
	s_setprio 0
	s_barrier
	ds_read_b128 v[32:35], v209 offset:49152
	ds_read_b128 v[36:39], v209 offset:50176
	ds_read_b128 v[40:43], v209 offset:51200
	ds_read_b128 v[44:47], v209 offset:52224
	ds_read_b128 v[48:51], v209 offset:53248
	ds_read_b128 v[52:55], v209 offset:54272
	ds_read_b128 v[56:59], v209 offset:55296
	ds_read_b128 v[60:63], v209 offset:56320
	s_mov_b32 m0, s69
	s_nop 0
	global_load_lds_dwordx4 v200, s[38:39]
	s_mov_b32 m0, s70
	s_nop 0
	global_load_lds_dwordx4 v202, s[38:39]
	s_add_u32 s38, s38, s16
	s_addc_u32 s39, s39, s17
	s_mov_b32 m0, s73
	s_nop 0
	global_load_lds_dwordx4 v200, s[38:39]
	s_mov_b32 m0, s74
	s_nop 0
	global_load_lds_dwordx4 v202, s[38:39]
	s_mov_b32 m0, s71
	s_nop 0
	global_load_lds_dwordx4 v64, s[8:9]
	s_mov_b32 m0, s72
	s_nop 0
	global_load_lds_dwordx4 v65, s[8:9]
	s_waitcnt vmcnt(8)
	s_waitcnt lgkmcnt(0)
	s_barrier
	s_setprio 1
	s_waitcnt lgkmcnt(6)
	v_mfma_scale_f32_16x16x128_f8f6f4 v[128:131], v[0:7], v[32:39], v[128:131], v210, v211 op_sel_hi:[0,0,0]
	v_mfma_scale_f32_16x16x128_f8f6f4 v[120:123], v[8:15], v[32:39], v[120:123], v210, v211 op_sel_hi:[0,0,0]
	s_waitcnt lgkmcnt(4)
	v_mfma_scale_f32_16x16x128_f8f6f4 v[112:115], v[0:7], v[40:47], v[112:115], v210, v211 op_sel_hi:[0,0,0]
	v_mfma_scale_f32_16x16x128_f8f6f4 v[104:107], v[8:15], v[40:47], v[104:107], v210, v211 op_sel_hi:[0,0,0]
	s_waitcnt lgkmcnt(2)
	v_mfma_scale_f32_16x16x128_f8f6f4 v[96:99], v[0:7], v[48:55], v[96:99], v210, v211 op_sel_hi:[0,0,0]
	v_mfma_scale_f32_16x16x128_f8f6f4 v[88:91], v[8:15], v[48:55], v[88:91], v210, v211 op_sel_hi:[0,0,0]
	s_waitcnt lgkmcnt(0)
	v_mfma_scale_f32_16x16x128_f8f6f4 v[80:83], v[0:7], v[56:63], v[80:83], v210, v211 op_sel_hi:[0,0,0]
	v_mfma_scale_f32_16x16x128_f8f6f4 v[72:75], v[8:15], v[56:63], v[72:75], v210, v211 op_sel_hi:[0,0,0]
	s_setprio 0
	s_setprio 1
	v_mfma_scale_f32_16x16x128_f8f6f4 v[124:127], v[16:23], v[32:39], v[124:127], v210, v211 op_sel_hi:[0,0,0]
	v_mfma_scale_f32_16x16x128_f8f6f4 v[116:119], v[24:31], v[32:39], v[116:119], v210, v211 op_sel_hi:[0,0,0]
	v_mfma_scale_f32_16x16x128_f8f6f4 v[108:111], v[16:23], v[40:47], v[108:111], v210, v211 op_sel_hi:[0,0,0]
	v_mfma_scale_f32_16x16x128_f8f6f4 v[100:103], v[24:31], v[40:47], v[100:103], v210, v211 op_sel_hi:[0,0,0]
	v_mfma_scale_f32_16x16x128_f8f6f4 v[92:95], v[16:23], v[48:55], v[92:95], v210, v211 op_sel_hi:[0,0,0]
	v_mfma_scale_f32_16x16x128_f8f6f4 v[84:87], v[24:31], v[48:55], v[84:87], v210, v211 op_sel_hi:[0,0,0]
	v_mfma_scale_f32_16x16x128_f8f6f4 v[76:79], v[16:23], v[56:63], v[76:79], v210, v211 op_sel_hi:[0,0,0]
	v_mfma_scale_f32_16x16x128_f8f6f4 v[68:71], v[24:31], v[56:63], v[68:71], v210, v211 op_sel_hi:[0,0,0]
	s_add_u32 s6, s6, 0x100
	s_addc_u32 s7, s7, 0
	s_cmp_ge_i32 s89, s68
	s_setprio 0
	s_barrier
	s_cbranch_scc1 .LBB0_1659

; #define PG8_STAGE(bufoff, gbase, voff) do { _Pragma("unroll") for (int _i = 0; _i < 2; ++_i) { unsigned keep_; \
;         asm volatile("s_mov_b32 %0, m0\n\ts_mov_b32 m0, %3\n\ts_nop 0\n\tglobal_load_lds_dwordx4 %1, %2\n\ts_mov_b32 m0, %0" : "=&s"(keep_) : "v"((voff)[_i]), "s"((const char*)(gbase)), "s"(ldsb + (unsigned)((bufoff) + _i * 8192)) : "memory"); } } while (0)
; #define PG8_LDA(dst, b, h) do { _Pragma("unroll") for (int m = 0; m < 4; ++m) _Pragma("unroll") for (int k = 0; k < 2; ++k) dst[m][k] = *(const PG8_LAS bf16x8*)(lds + PG8_SA(b, h) + aoff + m * 2048 + k * 1024); } while (0)
; #define PG8_LDB(dst, b, h) do { _Pragma("unroll") for (int n = 0; n < 2; ++n) _Pragma("unroll") for (int k = 0; k < 2; ++k) dst[n][k] = *(const PG8_LAS bf16x8*)(lds + PG8_SB(b, h) + boff + n * 2048 + k * 1024); } while (0)
; #define PG8_WAIT_V(n) asm volatile("s_waitcnt vmcnt(" #n ")" ::: "memory")
; #define PG8_WAIT_L(n) asm volatile("s_waitcnt lgkmcnt(" #n ")" ::: "memory")
; #define PG8_BAR __builtin_amdgcn_s_barrier()
; #define PG8_SCHED __builtin_amdgcn_sched_barrier(0)
; template <class Epi, class Sched, bool ALIGN_EPI, bool FP8 = false>
; __device__ __forceinline__ void gemm_phase(PG8_LAS unsigned char* lds, const Gemm g, const Sched& S, const Epi& E, const int wid, const int lane) {
;     ...
;         for (int t = 0; t < nt; t += 2) {
;             const bool last = (t == nt - 2);
;             const char* a1 = cA + (size_t)(t + 1) * kstep;
;             const char* a2 = last ? nA : cA + (size_t)(t + 2) * kstep; const char* b2 = last ? nB : cB + (size_t)(t + 2) * kstep;
;             const char* a3 = a2 + kstep; const char* b3 = b2 + kstep;
;             PG8_LDB(B0, 0, 0); PG8_LDB(B1, 0, 1); PG8_SCHED; PG8_LDA(At, 0, 0); PG8_STAGE(PG8_SA(1, 1), a1 + hstepA, vc1);
;             if (GA && last && has_next) { const u32x4 q = *gslot; vc0[0] = q.x; vc0[1] = q.y; vc1[0] = q.z; vc1[1] = q.w; }
;             PG8_WAIT_V(8); PG8_WAIT_L(0); PG8_BAR; PG8_MMA(0, 0, At, B0); PG8_MMA(0, 1, At, B1); PG8_BAR; PG8_SCHED;
;             PG8_LDA(At, 0, 1); PG8_STAGE(PG8_SB(0, 0), b2, voffB); PG8_STAGE(PG8_SB(0, 1), b2 + hstep, voffB); PG8_STAGE(PG8_SA(0, 0), a2, vc0);
;             PG8_WAIT_V(8); PG8_WAIT_L(0); PG8_BAR; PG8_MMA(1, 0, At, B0); PG8_MMA(1, 1, At, B1); PG8_BAR; PG8_SCHED;
.LBB0_1762:
	ds_read_b128 v[24:27], v165
	ds_read_b128 v[28:31], v165 offset:1024
	ds_read_b128 v[16:19], v165 offset:2048
	ds_read_b128 v[20:23], v165 offset:3072
	ds_read_b128 v[8:11], v167
	ds_read_b128 v[12:15], v167 offset:1024
	ds_read_b128 v[0:3], v167 offset:2048
	ds_read_b128 v[4:7], v167 offset:3072
	s_add_i32 s33, s8, 2
	s_cmp_eq_u32 s67, s8
	s_cselect_b32 s36, s28, s75
	s_cselect_b32 s37, s29, s80
	s_cselect_b32 s34, s30, s81
	s_cselect_b32 s35, s31, s82
	s_add_u32 s8, s36, 0x80
	s_addc_u32 s9, s37, 0
	ds_read_b128 v[174:177], v169
	ds_read_b128 v[178:181], v169 offset:1024
	ds_read_b128 v[182:185], v169 offset:2048
	ds_read_b128 v[186:189], v169 offset:3072
	ds_read_b128 v[190:193], v169 offset:4096
	ds_read_b128 v[194:197], v169 offset:5120
	ds_read_b128 v[198:201], v169 offset:6144
	ds_read_b128 v[202:205], v169 offset:7168
	s_mov_b32 m0, s68
	s_nop 0
	global_load_lds_dwordx4 v160, s[6:7]
	s_mov_b32 m0, s69
	s_nop 0
	global_load_lds_dwordx4 v164, s[6:7]
	s_waitcnt vmcnt(8)
	s_waitcnt lgkmcnt(0)
	s_barrier
	s_setprio 1
	s_waitcnt lgkmcnt(6)
	v_mfma_scale_f32_16x16x128_f8f6f4 v[156:159], v[24:31], v[174:181], v[156:159], v170, v171 op_sel_hi:[0,0,0]
	v_mfma_scale_f32_16x16x128_f8f6f4 v[152:155], v[16:23], v[174:181], v[152:155], v170, v171 op_sel_hi:[0,0,0]
	s_waitcnt lgkmcnt(4)
	v_mfma_scale_f32_16x16x128_f8f6f4 v[140:143], v[24:31], v[182:189], v[140:143], v170, v171 op_sel_hi:[0,0,0]
	v_mfma_scale_f32_16x16x128_f8f6f4 v[136:139], v[16:23], v[182:189], v[136:139], v170, v171 op_sel_hi:[0,0,0]
	s_waitcnt lgkmcnt(2)
	v_mfma_scale_f32_16x16x128_f8f6f4 v[124:127], v[24:31], v[190:197], v[124:127], v170, v171 op_sel_hi:[0,0,0]
	v_mfma_scale_f32_16x16x128_f8f6f4 v[120:123], v[16:23], v[190:197], v[120:123], v170, v171 op_sel_hi:[0,0,0]
	s_waitcnt lgkmcnt(0)
	v_mfma_scale_f32_16x16x128_f8f6f4 v[108:111], v[24:31], v[198:205], v[108:111], v170, v171 op_sel_hi:[0,0,0]
	v_mfma_scale_f32_16x16x128_f8f6f4 v[104:107], v[16:23], v[198:205], v[104:107], v170, v171 op_sel_hi:[0,0,0]
	s_setprio 0
	s_setprio 1
	v_mfma_scale_f32_16x16x128_f8f6f4 v[148:151], v[8:15], v[174:181], v[148:151], v170, v171 op_sel_hi:[0,0,0]
	v_mfma_scale_f32_16x16x128_f8f6f4 v[144:147], v[0:7], v[174:181], v[144:147], v170, v171 op_sel_hi:[0,0,0]
	v_mfma_scale_f32_16x16x128_f8f6f4 v[132:135], v[8:15], v[182:189], v[132:135], v170, v171 op_sel_hi:[0,0,0]
	v_mfma_scale_f32_16x16x128_f8f6f4 v[128:131], v[0:7], v[182:189], v[128:131], v170, v171 op_sel_hi:[0,0,0]
	v_mfma_scale_f32_16x16x128_f8f6f4 v[116:119], v[8:15], v[190:197], v[116:119], v170, v171 op_sel_hi:[0,0,0]
	v_mfma_scale_f32_16x16x128_f8f6f4 v[112:115], v[0:7], v[190:197], v[112:115], v170, v171 op_sel_hi:[0,0,0]
	v_mfma_scale_f32_16x16x128_f8f6f4 v[100:103], v[8:15], v[198:205], v[100:103], v170, v171 op_sel_hi:[0,0,0]
	v_mfma_scale_f32_16x16x128_f8f6f4 v[96:99], v[0:7], v[198:205], v[96:99], v170, v171 op_sel_hi:[0,0,0]
	s_setprio 0
	s_barrier
	ds_read_b128 v[174:177], v169 offset:16384
	ds_read_b128 v[178:181], v169 offset:17408
	ds_read_b128 v[182:185], v169 offset:18432
	ds_read_b128 v[186:189], v169 offset:19456
	ds_read_b128 v[190:193], v169 offset:20480
	ds_read_b128 v[194:197], v169 offset:21504
	ds_read_b128 v[198:201], v169 offset:22528
	ds_read_b128 v[202:205], v169 offset:23552
	s_mov_b32 m0, s45
	s_nop 0
	global_load_lds_dwordx4 v162, s[34:35]
	s_mov_b32 m0, s46
	s_nop 0
	global_load_lds_dwordx4 v166, s[34:35]
	s_add_u32 s58, s34, s12
	s_addc_u32 s59, s35, s13
	s_mov_b32 m0, s47
	s_nop 0
	global_load_lds_dwordx4 v162, s[58:59]
	s_mov_b32 m0, s48
	s_nop 0
	global_load_lds_dwordx4 v166, s[58:59]
	s_mov_b32 m0, s40
	s_nop 0
	global_load_lds_dwordx4 v160, s[36:37]
	s_mov_b32 m0, s49
	s_nop 0
	global_load_lds_dwordx4 v164, s[36:37]
	s_waitcnt vmcnt(8)
	s_waitcnt lgkmcnt(0)
	s_barrier
	s_setprio 1
	s_waitcnt lgkmcnt(6)
	v_mfma_scale_f32_16x16x128_f8f6f4 v[92:95], v[24:31], v[174:181], v[92:95], v170, v171 op_sel_hi:[0,0,0]
	v_mfma_scale_f32_16x16x128_f8f6f4 v[88:91], v[16:23], v[174:181], v[88:91], v170, v171 op_sel_hi:[0,0,0]
	s_waitcnt lgkmcnt(4)
	v_mfma_scale_f32_16x16x128_f8f6f4 v[76:79], v[24:31], v[182:189], v[76:79], v170, v171 op_sel_hi:[0,0,0]
	v_mfma_scale_f32_16x16x128_f8f6f4 v[72:75], v[16:23], v[182:189], v[72:75], v170, v171 op_sel_hi:[0,0,0]
	s_waitcnt lgkmcnt(2)
	v_mfma_scale_f32_16x16x128_f8f6f4 v[60:63], v[24:31], v[190:197], v[60:63], v170, v171 op_sel_hi:[0,0,0]
	v_mfma_scale_f32_16x16x128_f8f6f4 v[56:59], v[16:23], v[190:197], v[56:59], v170, v171 op_sel_hi:[0,0,0]
	s_waitcnt lgkmcnt(0)
	v_mfma_scale_f32_16x16x128_f8f6f4 v[44:47], v[24:31], v[198:205], v[44:47], v170, v171 op_sel_hi:[0,0,0]
	v_mfma_scale_f32_16x16x128_f8f6f4 v[40:43], v[16:23], v[198:205], v[40:43], v170, v171 op_sel_hi:[0,0,0]
	s_setprio 0
	s_setprio 1
	v_mfma_scale_f32_16x16x128_f8f6f4 v[84:87], v[8:15], v[174:181], v[84:87], v170, v171 op_sel_hi:[0,0,0]
	v_mfma_scale_f32_16x16x128_f8f6f4 v[80:83], v[0:7], v[174:181], v[80:83], v170, v171 op_sel_hi:[0,0,0]
	v_mfma_scale_f32_16x16x128_f8f6f4 v[68:71], v[8:15], v[182:189], v[68:71], v170, v171 op_sel_hi:[0,0,0]
	v_mfma_scale_f32_16x16x128_f8f6f4 v[64:67], v[0:7], v[182:189], v[64:67], v170, v171 op_sel_hi:[0,0,0]
	v_mfma_scale_f32_16x16x128_f8f6f4 v[52:55], v[8:15], v[190:197], v[52:55], v170, v171 op_sel_hi:[0,0,0]
	v_mfma_scale_f32_16x16x128_f8f6f4 v[48:51], v[0:7], v[190:197], v[48:51], v170, v171 op_sel_hi:[0,0,0]
	v_mfma_scale_f32_16x16x128_f8f6f4 v[36:39], v[8:15], v[198:205], v[36:39], v170, v171 op_sel_hi:[0,0,0]
	v_mfma_scale_f32_16x16x128_f8f6f4 v[32:35], v[0:7], v[198:205], v[32:35], v170, v171 op_sel_hi:[0,0,0]
	s_setprio 0
	s_barrier
; #define PG8_STAGE(bufoff, gbase, voff) do { _Pragma("unroll") for (int _i = 0; _i < 2; ++_i) { unsigned keep_; \
;         asm volatile("s_mov_b32 %0, m0\n\ts_mov_b32 m0, %3\n\ts_nop 0\n\tglobal_load_lds_dwordx4 %1, %2\n\ts_mov_b32 m0, %0" : "=&s"(keep_) : "v"((voff)[_i]), "s"((const char*)(gbase)), "s"(ldsb + (unsigned)((bufoff) + _i * 8192)) : "memory"); } } while (0)
; #define PG8_LDA(dst, b, h) do { _Pragma("unroll") for (int m = 0; m < 4; ++m) _Pragma("unroll") for (int k = 0; k < 2; ++k) dst[m][k] = *(const PG8_LAS bf16x8*)(lds + PG8_SA(b, h) + aoff + m * 2048 + k * 1024); } while (0)
; #define PG8_LDB(dst, b, h) do { _Pragma("unroll") for (int n = 0; n < 2; ++n) _Pragma("unroll") for (int k = 0; k < 2; ++k) dst[n][k] = *(const PG8_LAS bf16x8*)(lds + PG8_SB(b, h) + boff + n * 2048 + k * 1024); } while (0)
; #define PG8_WAIT_V(n) asm volatile("s_waitcnt vmcnt(" #n ")" ::: "memory")
; #define PG8_WAIT_L(n) asm volatile("s_waitcnt lgkmcnt(" #n ")" ::: "memory")
; #define PG8_BAR __builtin_amdgcn_s_barrier()
; #define PG8_SCHED __builtin_amdgcn_sched_barrier(0)
; template <class Epi, class Sched, bool ALIGN_EPI, bool FP8 = false>
; __device__ __forceinline__ void gemm_phase(PG8_LAS unsigned char* lds, const Gemm g, const Sched& S, const Epi& E, const int wid, const int lane) {
;     ...
;             PG8_LDB(B0, 1, 0); PG8_LDB(B1, 1, 1); PG8_SCHED; PG8_LDA(At, 1, 0); PG8_STAGE(PG8_SA(0, 1), a2 + hstepA, vc1);
;             PG8_WAIT_V(8); PG8_WAIT_L(0); PG8_BAR; PG8_MMA(0, 0, At, B0); PG8_MMA(0, 1, At, B1); PG8_BAR; PG8_SCHED;
;             PG8_LDA(At, 1, 1); PG8_STAGE(PG8_SB(1, 0), b3, voffB); PG8_STAGE(PG8_SB(1, 1), b3 + hstep, voffB); PG8_STAGE(PG8_SA(1, 0), a3, vc0);
;             PG8_WAIT_V(8); PG8_WAIT_L(0); PG8_BAR; PG8_MMA(1, 0, At, B0); PG8_MMA(1, 1, At, B1); PG8_BAR; PG8_SCHED;
;         }
	ds_read_b128 v[0:3], v172
	ds_read_b128 v[4:7], v172 offset:1024
	ds_read_b128 v[8:11], v172 offset:2048
	ds_read_b128 v[12:15], v172 offset:3072
	ds_read_b128 v[16:19], v173
	ds_read_b128 v[20:23], v173 offset:1024
	ds_read_b128 v[24:27], v173 offset:2048
	ds_read_b128 v[28:31], v173 offset:3072
	ds_read_b128 v[174:177], v169 offset:32768
	ds_read_b128 v[178:181], v169 offset:33792
	ds_read_b128 v[182:185], v169 offset:34816
	ds_read_b128 v[186:189], v169 offset:35840
	ds_read_b128 v[190:193], v169 offset:36864
	ds_read_b128 v[194:197], v169 offset:37888
	ds_read_b128 v[198:201], v169 offset:38912
	ds_read_b128 v[202:205], v169 offset:39936
	s_add_u32 s36, s36, s12
	s_addc_u32 s37, s37, s13
	s_mov_b32 m0, s50
	s_nop 0
	global_load_lds_dwordx4 v160, s[36:37]
	s_mov_b32 m0, s51
	s_nop 0
	global_load_lds_dwordx4 v164, s[36:37]
	s_waitcnt vmcnt(8)
	s_waitcnt lgkmcnt(0)
	s_barrier
	s_setprio 1
	s_waitcnt lgkmcnt(6)
	v_mfma_scale_f32_16x16x128_f8f6f4 v[156:159], v[0:7], v[174:181], v[156:159], v170, v171 op_sel_hi:[0,0,0]
	v_mfma_scale_f32_16x16x128_f8f6f4 v[152:155], v[8:15], v[174:181], v[152:155], v170, v171 op_sel_hi:[0,0,0]
	s_waitcnt lgkmcnt(4)
	v_mfma_scale_f32_16x16x128_f8f6f4 v[140:143], v[0:7], v[182:189], v[140:143], v170, v171 op_sel_hi:[0,0,0]
	v_mfma_scale_f32_16x16x128_f8f6f4 v[136:139], v[8:15], v[182:189], v[136:139], v170, v171 op_sel_hi:[0,0,0]
	s_waitcnt lgkmcnt(2)
	v_mfma_scale_f32_16x16x128_f8f6f4 v[124:127], v[0:7], v[190:197], v[124:127], v170, v171 op_sel_hi:[0,0,0]
	v_mfma_scale_f32_16x16x128_f8f6f4 v[120:123], v[8:15], v[190:197], v[120:123], v170, v171 op_sel_hi:[0,0,0]
	s_waitcnt lgkmcnt(0)
	v_mfma_scale_f32_16x16x128_f8f6f4 v[108:111], v[0:7], v[198:205], v[108:111], v170, v171 op_sel_hi:[0,0,0]
	v_mfma_scale_f32_16x16x128_f8f6f4 v[104:107], v[8:15], v[198:205], v[104:107], v170, v171 op_sel_hi:[0,0,0]
	s_setprio 0
	s_setprio 1
	v_mfma_scale_f32_16x16x128_f8f6f4 v[148:151], v[16:23], v[174:181], v[148:151], v170, v171 op_sel_hi:[0,0,0]
	v_mfma_scale_f32_16x16x128_f8f6f4 v[144:147], v[24:31], v[174:181], v[144:147], v170, v171 op_sel_hi:[0,0,0]
	v_mfma_scale_f32_16x16x128_f8f6f4 v[132:135], v[16:23], v[182:189], v[132:135], v170, v171 op_sel_hi:[0,0,0]
	v_mfma_scale_f32_16x16x128_f8f6f4 v[128:131], v[24:31], v[182:189], v[128:131], v170, v171 op_sel_hi:[0,0,0]
	v_mfma_scale_f32_16x16x128_f8f6f4 v[116:119], v[16:23], v[190:197], v[116:119], v170, v171 op_sel_hi:[0,0,0]
	v_mfma_scale_f32_16x16x128_f8f6f4 v[112:115], v[24:31], v[190:197], v[112:115], v170, v171 op_sel_hi:[0,0,0]
	v_mfma_scale_f32_16x16x128_f8f6f4 v[100:103], v[16:23], v[198:205], v[100:103], v170, v171 op_sel_hi:[0,0,0]
	v_mfma_scale_f32_16x16x128_f8f6f4 v[96:99], v[24:31], v[198:205], v[96:99], v170, v171 op_sel_hi:[0,0,0]
	s_setprio 0
	s_barrier
	ds_read_b128 v[174:177], v169 offset:49152
	ds_read_b128 v[178:181], v169 offset:50176
	ds_read_b128 v[182:185], v169 offset:51200
	ds_read_b128 v[186:189], v169 offset:52224
	ds_read_b128 v[190:193], v169 offset:53248
	ds_read_b128 v[194:197], v169 offset:54272
	ds_read_b128 v[198:201], v169 offset:55296
	ds_read_b128 v[202:205], v169 offset:56320
	s_add_u32 s34, s34, 0x80
	s_addc_u32 s35, s35, 0
	s_mov_b32 m0, s53
	s_nop 0
	global_load_lds_dwordx4 v162, s[34:35]
	s_mov_b32 m0, s54
	s_nop 0
	global_load_lds_dwordx4 v166, s[34:35]
	s_add_u32 s34, s34, s12
	s_addc_u32 s35, s35, s13
	s_mov_b32 m0, s65
	s_nop 0
	global_load_lds_dwordx4 v162, s[34:35]
	s_mov_b32 m0, s66
	s_nop 0
	global_load_lds_dwordx4 v166, s[34:35]
	s_mov_b32 m0, s55
	s_nop 0
	global_load_lds_dwordx4 v160, s[8:9]
	s_mov_b32 m0, s64
	s_nop 0
	global_load_lds_dwordx4 v164, s[8:9]
	s_waitcnt vmcnt(8)
	s_waitcnt lgkmcnt(0)
	s_barrier
	s_setprio 1
	s_waitcnt lgkmcnt(6)
	v_mfma_scale_f32_16x16x128_f8f6f4 v[92:95], v[0:7], v[174:181], v[92:95], v170, v171 op_sel_hi:[0,0,0]
	v_mfma_scale_f32_16x16x128_f8f6f4 v[88:91], v[8:15], v[174:181], v[88:91], v170, v171 op_sel_hi:[0,0,0]
	s_waitcnt lgkmcnt(4)
	v_mfma_scale_f32_16x16x128_f8f6f4 v[76:79], v[0:7], v[182:189], v[76:79], v170, v171 op_sel_hi:[0,0,0]
	v_mfma_scale_f32_16x16x128_f8f6f4 v[72:75], v[8:15], v[182:189], v[72:75], v170, v171 op_sel_hi:[0,0,0]
	s_waitcnt lgkmcnt(2)
	v_mfma_scale_f32_16x16x128_f8f6f4 v[60:63], v[0:7], v[190:197], v[60:63], v170, v171 op_sel_hi:[0,0,0]
	v_mfma_scale_f32_16x16x128_f8f6f4 v[56:59], v[8:15], v[190:197], v[56:59], v170, v171 op_sel_hi:[0,0,0]
	s_waitcnt lgkmcnt(0)
	v_mfma_scale_f32_16x16x128_f8f6f4 v[44:47], v[0:7], v[198:205], v[44:47], v170, v171 op_sel_hi:[0,0,0]
	v_mfma_scale_f32_16x16x128_f8f6f4 v[40:43], v[8:15], v[198:205], v[40:43], v170, v171 op_sel_hi:[0,0,0]
	s_setprio 0
	s_setprio 1
	v_mfma_scale_f32_16x16x128_f8f6f4 v[84:87], v[16:23], v[174:181], v[84:87], v170, v171 op_sel_hi:[0,0,0]
	v_mfma_scale_f32_16x16x128_f8f6f4 v[80:83], v[24:31], v[174:181], v[80:83], v170, v171 op_sel_hi:[0,0,0]
	v_mfma_scale_f32_16x16x128_f8f6f4 v[68:71], v[16:23], v[182:189], v[68:71], v170, v171 op_sel_hi:[0,0,0]
	v_mfma_scale_f32_16x16x128_f8f6f4 v[64:67], v[24:31], v[182:189], v[64:67], v170, v171 op_sel_hi:[0,0,0]
	v_mfma_scale_f32_16x16x128_f8f6f4 v[52:55], v[16:23], v[190:197], v[52:55], v170, v171 op_sel_hi:[0,0,0]
	v_mfma_scale_f32_16x16x128_f8f6f4 v[48:51], v[24:31], v[190:197], v[48:51], v170, v171 op_sel_hi:[0,0,0]
	v_mfma_scale_f32_16x16x128_f8f6f4 v[36:39], v[16:23], v[198:205], v[36:39], v170, v171 op_sel_hi:[0,0,0]
	v_mfma_scale_f32_16x16x128_f8f6f4 v[32:35], v[24:31], v[198:205], v[32:35], v170, v171 op_sel_hi:[0,0,0]
	s_add_u32 s75, s75, 0x100
	s_addc_u32 s80, s80, 0
	s_add_u32 s81, s81, 0x100
	s_addc_u32 s82, s82, 0
	s_add_u32 s6, s6, 0x100
	s_addc_u32 s7, s7, 0
	s_cmp_ge_i32 s33, s52
	s_mov_b32 s8, s33
	s_setprio 0
	s_barrier
	s_cbranch_scc0 .LBB0_1762
